# static s_setprio 1 for waves 4-7 before each GEMM K-loop, 64 per-segment flips removed (on top of v113 converters + P4 waits)
# baseline (speedup 1.0000x reference)
; #define PG8_STAGE_B(bufoff, gbase) do { _Pragma("unroll") for (int _i = 0; _i < 2; ++_i) \
;         __builtin_amdgcn_global_load_lds((const unsigned*)((const char*)(gbase) + voffB[_i]), (LAS unsigned*)(lds + (bufoff) + ldsw + _i * 8192), 16, 0, 0); } while (0)
; #define PG8_STAGE_A(bufoff, AO, h, kb) do { _Pragma("unroll") for (int _i = 0; _i < 2; ++_i) \
;         __builtin_amdgcn_global_load_lds((const unsigned*)(S.A + (size_t)(AO)[h][_i] + (size_t)(kb)), (LAS unsigned*)(lds + (bufoff) + ldsw + _i * 8192), 16, 0, 0); } while (0)
; #define PG8_WAIT_V(n) asm volatile("s_waitcnt vmcnt(" #n ")" ::: "memory")
; #define PG8_BAR __builtin_amdgcn_s_barrier()
; template <class P>
; __device__ __forceinline__ void gemm_phase(LAS unsigned char* lds, const P& S) {
;     ...
;     for (int i = 0; i < 2; ++i) { int R, C; stage_rc(tid * 16 + i * 8192, R, C); const int Rb = P::PERM ? ((R & ~31) + perm32(R & 31)) : R;
;         RA[i] = R; CA[i] = C; if constexpr (P::BBLK) voffB[i] = (unsigned)((C >> 3) * S.NB + Rb) * 16u; else voffB[i] = (unsigned)(Rb * K + C) * 2u; }
;     const size_t kstep = (size_t)(BK * 2);
;     size_t kstepB = kstep; if constexpr (P::BBLK) kstepB = (size_t)128 * (size_t)S.NB;
;     const unsigned ldsw = (unsigned)wid * 1024u;
;     const int aoff = lds_byte(wr * 64 + fr, fq * 8), boff = lds_byte(wc * 32 + fr, fq * 8);
;     ...
; typedef int i32x2 __attribute__((ext_vector_type(2)));
;     ...
;     Unit cur, nxt; int ui = 0;
;     if (!S.next(0, cur)) return;
;     f32x4 acc[2][2][4][2];
; #pragma unroll
;     for (int a = 0; a < 2; ++a)
; #pragma unroll
;         for (int b = 0; b < 2; ++b)
; #pragma unroll
;             for (int m = 0; m < 4; ++m)
; #pragma unroll
;                 for (int n = 0; n < 2; ++n) acc[a][b][m][n] = (f32x4){0.f, 0.f, 0.f, 0.f};
;     i32x8 At[4], B0[2], B1[2];
;     unsigned ac[2][2], a2[2][2];
;     PG8_AOFF(ac, cur, 0);
;     const char* cB0 = S.bptr(cur, 0); const char* cB1 = S.bptr(cur, 1);
;     PG8_STAGE_B(PG8_SB(0, 0), cB0); PG8_STAGE_A(PG8_SA(0, 0), ac, 0, 0); PG8_STAGE_B(PG8_SB(0, 1), cB1); PG8_STAGE_A(PG8_SA(0, 1), ac, 1, 0);
;     if (wr == 1) PG8_BAR;
;     PG8_WAIT_V(4); PG8_BAR;
;     PG8_STAGE_B(PG8_SB(1, 0), cB0 + kstepB); PG8_STAGE_A(PG8_SA(1, 0), ac, 0, kstep); PG8_STAGE_B(PG8_SB(1, 1), cB1 + kstepB);
;     PG8_WAIT_V(6); PG8_BAR;
.LBB0_207:
	s_andn2_b64 vcc, exec, s[4:5]
	s_cbranch_vccnz .LBB0_227
	s_waitcnt vmcnt(16)
	v_mov_b32_e32 v14, v0
	s_cmpk_gt_i32 s80, 0x759
	v_readfirstlane_b32 s27, v14
	s_cbranch_scc1 .LBB0_227
	s_ashr_i32 s2, s80, 31
	s_lshr_b32 s2, s2, 29
	s_add_i32 s2, s80, s2
	s_and_b32 s3, s2, -8
	s_sub_i32 s3, s80, s3
	s_cmp_lt_i32 s3, 0
	s_movk_i32 s28, 0xe9
	v_ashrrev_i32_e32 v1, 31, v14
	s_cselect_b32 s4, s28, 0xe8
	v_lshrrev_b32_e32 v1, 26, v1
	s_mul_i32 s3, s4, s3
	s_ashr_i32 s2, s2, 3
	v_add_u32_e32 v1, v14, v1
	s_add_i32 s3, s3, s2
	v_ashrrev_i32_e32 v3, 6, v1
	v_bfe_i32 v1, v14, 27, 1
	s_mul_hi_i32 s2, s3, 0x8d3dcb09
	v_lshlrev_b32_e32 v2, 4, v14
	v_lshrrev_b32_e32 v1, 22, v1
	s_add_i32 s2, s2, s3
	v_add_u32_e32 v1, v2, v1
	s_lshr_b32 s4, s2, 31
	s_ashr_i32 s2, s2, 7
	v_and_b32_e32 v1, 0xfffffc00, v1
	s_add_i32 s2, s2, s4
	v_sub_u32_e32 v1, v2, v1
	v_add_u32_e32 v2, 0x2000, v2
	s_mul_i32 s4, s2, 0xe8
	v_ashrrev_i32_e32 v7, 31, v2
	s_sub_i32 s3, s3, s4
	v_lshrrev_b32_e32 v7, 22, v7
	s_sext_i32_i16 s4, s3
	v_add_u32_e32 v7, v2, v7
	s_bfe_u32 s4, s4, 0x3001c
	v_ashrrev_i32_e32 v7, 10, v7
	s_add_i32 s4, s3, s4
	v_mul_i32_i24_e32 v8, 0x400, v7
	s_sext_i32_i16 s5, s4
	s_and_b32 s4, s4, 0xfff8
	v_sub_u32_e32 v2, v2, v8
	s_sub_i32 s3, s3, s4
	v_lshrrev_b32_e32 v8, 4, v2
	s_sext_i32_i16 s3, s3
	s_lshl_b32 s2, s2, 3
	v_lshrrev_b32_e32 v4, 4, v1
	v_bitop3_b32 v2, v8, v2, 32 bitop3:0x6c
	s_ashr_i32 s5, s5, 3
	s_add_i32 s2, s2, s3
	s_add_i32 s3, s80, 0xfffff8c0
	s_add_i32 s4, s80, 0xfffff8b3
	v_bitop3_b32 v4, v4, v1, 32 bitop3:0x6c
	v_ashrrev_i32_e32 v9, 31, v2
	s_cmp_lt_u32 s3, 13
	v_ashrrev_i32_e32 v5, 31, v4
	v_lshrrev_b32_e32 v9, 26, v9
	s_cselect_b32 s6, s3, s4
	s_cmp_gt_u32 s3, 12
	v_lshrrev_b32_e32 v5, 26, v5
	v_lshlrev_b32_e32 v8, 3, v7
	v_add_u32_e32 v9, v2, v9
	s_cselect_b32 s3, 0x41, 64
	s_ashr_i32 s4, s27, 6
	v_add_u32_e32 v5, v4, v5
	v_and_b32_e32 v8, -16, v8
	v_ashrrev_i32_e32 v10, 6, v9
	s_ashr_i32 s8, s27, 8
	s_lshl_b32 s29, s4, 10
	v_ashrrev_i32_e32 v6, 6, v5
	v_add_u32_e32 v150, v10, v8
	v_and_b32_e32 v8, 0xc0, v9
	v_and_b32_e32 v5, 0xc0, v5
	s_cmpk_lt_i32 s80, 0x740
	v_sub_u32_e32 v2, v2, v8
	v_mov_b32_e32 v8, 1
	v_sub_u32_e32 v4, v4, v5
	v_lshlrev_b32_e32 v1, 3, v3
	s_cselect_b32 s46, s5, s6
	v_lshlrev_b32_e32 v7, 5, v7
	v_ashrrev_i16_sdwa v2, v8, sext(v2) dst_sel:DWORD dst_unused:UNUSED_PAD src0_sel:DWORD src1_sel:BYTE_0
	v_ashrrev_i16_sdwa v4, v8, sext(v4) dst_sel:DWORD dst_unused:UNUSED_PAD src0_sel:DWORD src1_sel:BYTE_0
	v_and_b32_e32 v5, 3, v10
	s_mov_b32 s5, 0xfffe0
	v_lshrrev_b32_e32 v8, 2, v150
	v_lshlrev_b32_e32 v9, 1, v150
	v_and_b32_e32 v1, -16, v1
	v_and_b32_e32 v7, 32, v7
	v_bfe_i32 v2, v2, 0, 16
	v_and_or_b32 v5, v150, s5, v5
	v_and_b32_e32 v8, 4, v8
	v_and_b32_e32 v9, 24, v9
	v_add_u32_e32 v1, v6, v1
	s_cselect_b32 s45, s2, s3
	s_add_u32 s2, s86, 0x33000000
	v_or3_b32 v5, v5, v8, v9
	v_add_lshl_u32 v151, v7, v2, 1
	s_addc_u32 s3, s87, 0
	v_lshlrev_b32_e32 v3, 5, v3
	v_lshl_add_u32 v130, v5, 12, v151
	v_and_b32_e32 v2, 3, v6
	v_lshrrev_b32_e32 v5, 2, v1
	v_lshlrev_b32_e32 v6, 1, v1
	s_add_u32 s30, s86, 0x800000
	v_and_b32_e32 v3, 32, v3
	v_bfe_i32 v4, v4, 0, 16
	v_and_or_b32 v2, v1, s5, v2
	v_and_b32_e32 v5, 4, v5
	v_and_b32_e32 v6, 24, v6
	s_addc_u32 s31, s87, 0
	v_or3_b32 v2, v2, v5, v6
	v_add_lshl_u32 v152, v3, v4, 1
	s_lshl_b32 s5, s45, 8
	s_lshl_b32 s6, s46, 8
	v_lshl_add_u32 v132, v2, 12, v152
	v_add_u32_e32 v2, s5, v1
	s_ashr_i32 s7, s6, 31
	v_lshl_add_u32 v136, v2, 12, v152
	v_add_u32_e32 v2, s5, v150
	s_bitset1_b32 s5, 7
	s_lshl_b64 s[10:11], s[6:7], 12
	s_add_u32 s18, s30, s10
	s_addc_u32 s19, s31, s11
	s_add_i32 s33, s29, 0
	s_bitset1_b32 s6, 7
	s_add_i32 m0, s33, 0x10000
	s_ashr_i32 s7, s6, 31
	global_load_lds_dwordx4 v132, s[18:19]
	s_add_i32 m0, s33, 0x12000
	s_lshl_b64 s[6:7], s[6:7], 12
	global_load_lds_dwordx4 v130, s[18:19]
	s_mov_b32 m0, s33
	s_add_i32 s34, s33, 0x2000
	v_lshl_add_u32 v138, v2, 12, v151
	global_load_lds_dwordx4 v136, s[2:3]
	s_mov_b32 m0, s34
	s_add_u32 s20, s30, s6
	global_load_lds_dwordx4 v138, s[2:3]
	s_addc_u32 s21, s31, s7
	s_add_i32 m0, s33, 0x14000
	v_add_u32_e32 v2, s5, v1
	global_load_lds_dwordx4 v132, s[20:21]
	s_add_i32 m0, s33, 0x16000
	s_add_i32 s35, s33, 0x4000
	v_lshl_add_u32 v140, v2, 12, v152
	v_add_u32_e32 v2, s5, v150
	global_load_lds_dwordx4 v130, s[20:21]
	s_mov_b32 m0, s35
	s_add_i32 s36, s33, 0x6000
	v_lshl_add_u32 v142, v2, 12, v151
	global_load_lds_dwordx4 v140, s[2:3]
	s_mov_b32 m0, s36
	v_mov_b32_e32 v135, 0
	global_load_lds_dwordx4 v142, s[2:3]
	v_mov_b32_e32 v133, v135
	v_mov_b32_e32 v131, v135
	v_mov_b32_e32 v137, v135
	v_mov_b32_e32 v139, v135
	s_mov_b32 s37, 0
	v_lshl_add_u64 v[12:13], s[18:19], 0, v[132:133]
	v_lshl_add_u64 v[10:11], s[18:19], 0, v[130:131]
	v_lshl_add_u64 v[8:9], s[2:3], 0, v[136:137]
	v_lshl_add_u64 v[6:7], s[2:3], 0, v[138:139]
	v_lshl_add_u64 v[4:5], s[20:21], 0, v[132:133]
	s_cmp_lg_u32 s8, 1
	v_lshl_add_u64 v[2:3], s[20:21], 0, v[130:131]
	s_cbranch_scc1 .LBB0_211
	s_setprio 1
	s_barrier

; #define PG8_STAGE_B(bufoff, gbase) do { _Pragma("unroll") for (int _i = 0; _i < 2; ++_i) \
;         __builtin_amdgcn_global_load_lds((const unsigned*)((const char*)(gbase) + voffB[_i]), (LAS unsigned*)(lds + (bufoff) + ldsw + _i * 8192), 16, 0, 0); } while (0)
; #define PG8_WAIT_V(n) asm volatile("s_waitcnt vmcnt(" #n ")" ::: "memory")
; template <class P>
; __device__ __forceinline__ void gemm_phase(LAS unsigned char* lds, const P& S) {
;     ...
;         for (int t = 0; t < nt; t += 2) {
;             const bool last = (t == nt - 2);
;             if (last) { S.bias_issue(cur, lds + BIAS_OFF, wid, lane); pre = S.prefetch(cur, wr, wc, fr, fq); }
;             if (last && has_next) { PG8_AOFF(a2, nxt, ui + 1); } else {
; #pragma unroll
;                 for (int _h = 0; _h < 2; ++_h)
; #pragma unroll
;                     for (int _i = 0; _i < 2; ++_i) a2[_h][_i] = last ? ac[_h][_i] : ac[_h][_i] + (unsigned)((t + 2) * (BK * 2)); }
;             const size_t k1 = (size_t)(t + 1) * kstep;
;             const char* b20 = last ? nB0 : cB0 + (size_t)(t + 2) * kstepB; const char* b21 = last ? nB1 : cB1 + (size_t)(t + 2) * kstepB;
;             PG8_LDB(B0, 0, 0); PG8_SCHED; PG8_LDA(At, 0, 0); PG8_STAGE_A(PG8_SA(1, 1), ac, 1, k1);
;             PG8_WAIT_L(8); PG8_BAR; PG8_WAIT_L(0); PG8_MMA(0, 0, At, B0); PG8_BAR; PG8_SCHED;
;             PG8_LDB(B1, 0, 1); PG8_STAGE_B(PG8_SB(0, 0), b20);
;             PG8_BAR; PG8_WAIT_L(0); PG8_MMA(0, 1, At, B1); PG8_BAR;
;             PG8_LDA(At, 0, 1); PG8_STAGE_A(PG8_SA(0, 0), a2, 0, 0);
;             PG8_BAR; PG8_WAIT_L(0); PG8_MMA(1, 0, At, B0); PG8_BAR; PG8_SCHED;
;             PG8_STAGE_B(PG8_SB(0, 1), b21);
;             PG8_WAIT_V(6); PG8_BAR; PG8_MMA(1, 1, At, B1); PG8_BAR;
;             PG8_LDB(B0, 1, 0); PG8_SCHED; PG8_LDA(At, 1, 0); PG8_STAGE_A(PG8_SA(0, 1), a2, 1, 0);
;             PG8_WAIT_L(8); PG8_BAR; PG8_WAIT_L(0); PG8_MMA(0, 0, At, B0); PG8_BAR; PG8_SCHED;
;             PG8_LDB(B1, 1, 1); PG8_STAGE_B(PG8_SB(1, 0), b20 + kstepB);
;             PG8_BAR; PG8_WAIT_L(0); PG8_MMA(0, 1, At, B1); PG8_BAR;
;             PG8_LDA(At, 1, 1); PG8_STAGE_A(PG8_SA(1, 0), a2, 0, kstep);
;             PG8_BAR; PG8_WAIT_L(0); PG8_MMA(1, 0, At, B0); PG8_BAR; PG8_SCHED;
;             PG8_STAGE_B(PG8_SB(1, 1), b21 + kstepB);
;             PG8_WAIT_V(6); PG8_BAR; PG8_MMA(1, 1, At, B1); PG8_BAR;
.LBB0_219:
	v_add_u32_e32 v145, s40, v154
	ds_read_b128 v[164:167], v145
	ds_read_b128 v[168:171], v145 offset:1024
	ds_read_b128 v[172:175], v145 offset:2048
	ds_read_b128 v[176:179], v145 offset:3072
	s_add_u32 s54, s49, s20
	s_addc_u32 s55, s50, s21
	s_add_u32 s56, s51, s20
	s_addc_u32 s57, s52, s21
	s_and_b64 s[24:25], s[22:23], exec
	s_cselect_b32 s25, s47, s55
	s_cselect_b32 s24, s48, s54
	v_lshl_add_u64 v[160:161], v[146:147], 0, s[20:21]
	s_add_i32 m0, s33, 0xc000
	ds_read_b128 v[180:183], v156
	ds_read_b128 v[184:187], v156 offset:1024
	ds_read_b128 v[188:191], v156 offset:2048
	ds_read_b128 v[192:195], v156 offset:3072
	ds_read_b128 v[196:199], v156 offset:4096
	ds_read_b128 v[200:203], v156 offset:5120
	ds_read_b128 v[204:207], v156 offset:6144
	ds_read_b128 v[208:211], v156 offset:7168
	global_load_lds_dwordx4 v[160:161], off
	v_lshl_add_u64 v[160:161], v[148:149], 0, s[20:21]
	s_add_i32 m0, s33, 0xe000
	s_nop 0
	global_load_lds_dwordx4 v[160:161], off
	s_waitcnt lgkmcnt(8)
	s_barrier
	s_waitcnt lgkmcnt(0)
	s_nop 0
	s_waitcnt lgkmcnt(0)
	v_mfma_f32_16x16x32_bf16 v[126:129], v[164:167], v[180:183], v[126:129]
	v_mfma_f32_16x16x32_bf16 v[122:125], v[172:175], v[180:183], v[122:125]
	v_mfma_f32_16x16x32_bf16 v[118:121], v[164:167], v[188:191], v[118:121]
	v_mfma_f32_16x16x32_bf16 v[110:113], v[172:175], v[188:191], v[110:113]
	v_mfma_f32_16x16x32_bf16 v[102:105], v[164:167], v[196:199], v[102:105]
	v_mfma_f32_16x16x32_bf16 v[94:97], v[172:175], v[196:199], v[94:97]
	v_mfma_f32_16x16x32_bf16 v[86:89], v[164:167], v[204:207], v[86:89]
	v_mfma_f32_16x16x32_bf16 v[78:81], v[172:175], v[204:207], v[78:81]
	v_mfma_f32_16x16x32_bf16 v[126:129], v[168:171], v[184:187], v[126:129]
	v_mfma_f32_16x16x32_bf16 v[122:125], v[176:179], v[184:187], v[122:125]
	v_mfma_f32_16x16x32_bf16 v[118:121], v[168:171], v[192:195], v[118:121]
	v_mfma_f32_16x16x32_bf16 v[110:113], v[176:179], v[192:195], v[110:113]
	v_mfma_f32_16x16x32_bf16 v[102:105], v[168:171], v[200:203], v[102:105]
	v_mfma_f32_16x16x32_bf16 v[94:97], v[176:179], v[200:203], v[94:97]
	v_mfma_f32_16x16x32_bf16 v[86:89], v[168:171], v[208:211], v[86:89]
	v_mfma_f32_16x16x32_bf16 v[78:81], v[176:179], v[208:211], v[78:81]
	s_nop 0
	s_barrier
	s_add_i32 s20, s40, s29
	v_add_u32_e32 v145, s41, v154
	v_lshl_add_u64 v[160:161], s[24:25], 0, v[132:133]
	s_mov_b32 m0, s20
	ds_read_b128 v[212:215], v145
	ds_read_b128 v[216:219], v145 offset:1024
	ds_read_b128 v[220:223], v145 offset:2048
	ds_read_b128 v[224:227], v145 offset:3072
	global_load_lds_dwordx4 v[160:161], off
	v_lshl_add_u64 v[228:229], s[24:25], 0, v[130:131]
	s_add_i32 m0, s20, 0x2000
	s_nop 0
	global_load_lds_dwordx4 v[228:229], off
	s_barrier
	s_waitcnt lgkmcnt(0)
	s_nop 0
	s_waitcnt lgkmcnt(0)
	v_mfma_f32_16x16x32_bf16 v[114:117], v[212:215], v[180:183], v[114:117]
	v_mfma_f32_16x16x32_bf16 v[106:109], v[220:223], v[180:183], v[106:109]
	v_mfma_f32_16x16x32_bf16 v[98:101], v[212:215], v[188:191], v[98:101]
	v_mfma_f32_16x16x32_bf16 v[90:93], v[220:223], v[188:191], v[90:93]
	v_mfma_f32_16x16x32_bf16 v[82:85], v[212:215], v[196:199], v[82:85]
	v_mfma_f32_16x16x32_bf16 v[74:77], v[220:223], v[196:199], v[74:77]
	v_mfma_f32_16x16x32_bf16 v[70:73], v[212:215], v[204:207], v[70:73]
	v_mfma_f32_16x16x32_bf16 v[66:69], v[220:223], v[204:207], v[66:69]
	v_mfma_f32_16x16x32_bf16 v[114:117], v[216:219], v[184:187], v[114:117]
	v_mfma_f32_16x16x32_bf16 v[106:109], v[224:227], v[184:187], v[106:109]
	v_mfma_f32_16x16x32_bf16 v[98:101], v[216:219], v[192:195], v[98:101]
	v_mfma_f32_16x16x32_bf16 v[90:93], v[224:227], v[192:195], v[90:93]
	v_mfma_f32_16x16x32_bf16 v[82:85], v[216:219], v[200:203], v[82:85]
	v_mfma_f32_16x16x32_bf16 v[74:77], v[224:227], v[200:203], v[74:77]
	v_mfma_f32_16x16x32_bf16 v[70:73], v[216:219], v[208:211], v[70:73]
	v_mfma_f32_16x16x32_bf16 v[66:69], v[224:227], v[208:211], v[66:69]
	s_nop 0
	s_mov_b32 m0, s33
	s_barrier
	ds_read_b128 v[180:183], v156 offset:16384
	ds_read_b128 v[184:187], v156 offset:17408
	ds_read_b128 v[188:191], v156 offset:18432
	ds_read_b128 v[192:195], v156 offset:19456
	ds_read_b128 v[196:199], v156 offset:20480
	ds_read_b128 v[200:203], v156 offset:21504
	ds_read_b128 v[204:207], v156 offset:22528
	ds_read_b128 v[208:211], v156 offset:23552
	global_load_lds_dwordx4 v134, s[2:3]
	s_mov_b32 m0, s34
	v_mov_b32_e32 v145, v135
	global_load_lds_dwordx4 v144, s[2:3]
	s_barrier
	s_waitcnt lgkmcnt(0)
	v_lshl_add_u64 v[230:231], s[2:3], 0, v[134:135]
	v_lshl_add_u64 v[232:233], s[2:3], 0, v[144:145]
	s_nop 0
	s_waitcnt lgkmcnt(0)
	v_mfma_f32_16x16x32_bf16 v[62:65], v[164:167], v[180:183], v[62:65]
	s_and_b64 s[20:21], s[22:23], exec
	s_cselect_b32 s21, s15, s57
	s_cselect_b32 s20, s14, s56
	v_mfma_f32_16x16x32_bf16 v[58:61], v[172:175], v[180:183], v[58:61]
	v_mfma_f32_16x16x32_bf16 v[54:57], v[164:167], v[188:191], v[54:57]
	v_mfma_f32_16x16x32_bf16 v[50:53], v[172:175], v[188:191], v[50:53]
	v_mfma_f32_16x16x32_bf16 v[38:41], v[164:167], v[196:199], v[38:41]
	v_mfma_f32_16x16x32_bf16 v[34:37], v[172:175], v[196:199], v[34:37]
	v_mfma_f32_16x16x32_bf16 v[22:25], v[164:167], v[204:207], v[22:25]
	v_mfma_f32_16x16x32_bf16 v[18:21], v[172:175], v[204:207], v[18:21]
	v_mfma_f32_16x16x32_bf16 v[62:65], v[168:171], v[184:187], v[62:65]
	v_mfma_f32_16x16x32_bf16 v[58:61], v[176:179], v[184:187], v[58:61]
	v_mfma_f32_16x16x32_bf16 v[54:57], v[168:171], v[192:195], v[54:57]
	v_mfma_f32_16x16x32_bf16 v[50:53], v[176:179], v[192:195], v[50:53]
	v_mfma_f32_16x16x32_bf16 v[38:41], v[168:171], v[200:203], v[38:41]
	v_mfma_f32_16x16x32_bf16 v[34:37], v[176:179], v[200:203], v[34:37]
	v_mfma_f32_16x16x32_bf16 v[22:25], v[168:171], v[208:211], v[22:25]
	v_mfma_f32_16x16x32_bf16 v[18:21], v[176:179], v[208:211], v[18:21]
	s_nop 0
	s_barrier
; #define PG8_STAGE_B(bufoff, gbase) do { _Pragma("unroll") for (int _i = 0; _i < 2; ++_i) \
;         __builtin_amdgcn_global_load_lds((const unsigned*)((const char*)(gbase) + voffB[_i]), (LAS unsigned*)(lds + (bufoff) + ldsw + _i * 8192), 16, 0, 0); } while (0)
; #define PG8_STAGE_A(bufoff, AO, h, kb) do { _Pragma("unroll") for (int _i = 0; _i < 2; ++_i) \
;         __builtin_amdgcn_global_load_lds((const unsigned*)(S.A + (size_t)(AO)[h][_i] + (size_t)(kb)), (LAS unsigned*)(lds + (bufoff) + ldsw + _i * 8192), 16, 0, 0); } while (0)
; #define PG8_LDA(dst, b, h) do { _Pragma("unroll") for (int m = 0; m < 4; ++m) { dst[m].lo = *(const LAS i32x4*)(lds + PG8_SA(b, h) + aoff + m * 2048); dst[m].hi = *(const LAS i32x4*)(lds + PG8_SA(b, h) + aoff + m * 2048 + 1024); } } while (0)
; #define PG8_LDB(dst, b, h) do { _Pragma("unroll") for (int n = 0; n < 2; ++n) { dst[n].lo = *(const LAS i32x4*)(lds + PG8_SB(b, h) + boff + n * 2048); dst[n].hi = *(const LAS i32x4*)(lds + PG8_SB(b, h) + boff + n * 2048 + 1024); } } while (0)
; #define PG8_WAIT_V(n) asm volatile("s_waitcnt vmcnt(" #n ")" ::: "memory")
; #define PG8_WAIT_L(n) asm volatile("s_waitcnt lgkmcnt(" #n ")" ::: "memory")
; #define PG8_BAR __builtin_amdgcn_s_barrier()
; #define PG8_SCHED __builtin_amdgcn_sched_barrier(0)
; template <class P>
; __device__ __forceinline__ void gemm_phase(LAS unsigned char* lds, const P& S) {
;     ...
;             PG8_LDA(At, 0, 1); PG8_STAGE_A(PG8_SA(0, 0), a2, 0, 0);
;             PG8_BAR; PG8_WAIT_L(0); PG8_MMA(1, 0, At, B0); PG8_BAR; PG8_SCHED;
;             PG8_STAGE_B(PG8_SB(0, 1), b21);
;             PG8_WAIT_V(6); PG8_BAR; PG8_MMA(1, 1, At, B1); PG8_BAR;
;             PG8_LDB(B0, 1, 0); PG8_SCHED; PG8_LDA(At, 1, 0); PG8_STAGE_A(PG8_SA(0, 1), a2, 1, 0);
;             PG8_WAIT_L(8); PG8_BAR; PG8_WAIT_L(0); PG8_MMA(0, 0, At, B0); PG8_BAR; PG8_SCHED;
;             PG8_LDB(B1, 1, 1); PG8_STAGE_B(PG8_SB(1, 0), b20 + kstepB);
;             PG8_BAR; PG8_WAIT_L(0); PG8_MMA(0, 1, At, B1); PG8_BAR;
;             PG8_LDA(At, 1, 1); PG8_STAGE_A(PG8_SA(1, 0), a2, 0, kstep);
;             PG8_BAR; PG8_WAIT_L(0); PG8_MMA(1, 0, At, B0); PG8_BAR; PG8_SCHED;
;             PG8_STAGE_B(PG8_SB(1, 1), b21 + kstepB);
;             PG8_WAIT_V(6); PG8_BAR; PG8_MMA(1, 1, At, B1); PG8_BAR;
	s_add_i32 s22, s41, s29
	v_lshl_add_u64 v[234:235], s[20:21], 0, v[132:133]
	s_mov_b32 m0, s22
	v_lshl_add_u64 v[236:237], s[20:21], 0, v[130:131]
	global_load_lds_dwordx4 v[234:235], off
	s_add_i32 m0, s22, 0x2000
	s_nop 0
	global_load_lds_dwordx4 v[236:237], off
	s_waitcnt vmcnt(6)
	s_barrier
	s_nop 0
	v_mfma_f32_16x16x32_bf16 v[46:49], v[212:215], v[180:183], v[46:49]
	v_mfma_f32_16x16x32_bf16 v[42:45], v[220:223], v[180:183], v[42:45]
	v_mfma_f32_16x16x32_bf16 v[30:33], v[212:215], v[188:191], v[30:33]
	v_mfma_f32_16x16x32_bf16 v[26:29], v[220:223], v[188:191], v[26:29]
	v_mfma_f32_16x16x32_bf16 v[14:17], v[212:215], v[196:199], v[14:17]
	v_mfma_f32_16x16x32_bf16 v[10:13], v[220:223], v[196:199], v[10:13]
	v_mfma_f32_16x16x32_bf16 v[6:9], v[212:215], v[204:207], v[6:9]
	v_mfma_f32_16x16x32_bf16 v[2:5], v[220:223], v[204:207], v[2:5]
	v_mfma_f32_16x16x32_bf16 v[46:49], v[216:219], v[184:187], v[46:49]
	v_mfma_f32_16x16x32_bf16 v[42:45], v[224:227], v[184:187], v[42:45]
	v_mfma_f32_16x16x32_bf16 v[30:33], v[216:219], v[192:195], v[30:33]
	v_mfma_f32_16x16x32_bf16 v[26:29], v[224:227], v[192:195], v[26:29]
	v_mfma_f32_16x16x32_bf16 v[14:17], v[216:219], v[200:203], v[14:17]
	v_mfma_f32_16x16x32_bf16 v[10:13], v[224:227], v[200:203], v[10:13]
	v_mfma_f32_16x16x32_bf16 v[6:9], v[216:219], v[208:211], v[6:9]
	v_mfma_f32_16x16x32_bf16 v[2:5], v[224:227], v[208:211], v[2:5]
	s_nop 0
	s_add_i32 s20, 0, 0x18000
	v_add_u32_e32 v145, s20, v154
	s_barrier
	ds_read_b128 v[164:167], v145
	ds_read_b128 v[168:171], v145 offset:1024
	ds_read_b128 v[172:175], v145 offset:2048
	ds_read_b128 v[176:179], v145 offset:3072
	s_mov_b32 m0, s35
	ds_read_b128 v[180:183], v156 offset:32768
	ds_read_b128 v[184:187], v156 offset:33792
	ds_read_b128 v[188:191], v156 offset:34816
	ds_read_b128 v[192:195], v156 offset:35840
	ds_read_b128 v[196:199], v156 offset:36864
	ds_read_b128 v[200:203], v156 offset:37888
	ds_read_b128 v[204:207], v156 offset:38912
	ds_read_b128 v[208:211], v156 offset:39936
	global_load_lds_dwordx4 v143, s[2:3]
	s_mov_b32 m0, s36
	s_nop 0
	global_load_lds_dwordx4 v141, s[2:3]
	s_waitcnt lgkmcnt(8)
	s_barrier
	s_waitcnt lgkmcnt(0)
	s_nop 0
	s_waitcnt lgkmcnt(0)
	v_mfma_f32_16x16x32_bf16 v[126:129], v[164:167], v[180:183], v[126:129]
	v_mfma_f32_16x16x32_bf16 v[122:125], v[172:175], v[180:183], v[122:125]
	v_mfma_f32_16x16x32_bf16 v[118:121], v[164:167], v[188:191], v[118:121]
	v_mfma_f32_16x16x32_bf16 v[110:113], v[172:175], v[188:191], v[110:113]
	v_mfma_f32_16x16x32_bf16 v[102:105], v[164:167], v[196:199], v[102:105]
	v_mfma_f32_16x16x32_bf16 v[94:97], v[172:175], v[196:199], v[94:97]
	v_mfma_f32_16x16x32_bf16 v[86:89], v[164:167], v[204:207], v[86:89]
	v_mfma_f32_16x16x32_bf16 v[78:81], v[172:175], v[204:207], v[78:81]
	v_mfma_f32_16x16x32_bf16 v[126:129], v[168:171], v[184:187], v[126:129]
	v_mfma_f32_16x16x32_bf16 v[122:125], v[176:179], v[184:187], v[122:125]
	v_mfma_f32_16x16x32_bf16 v[118:121], v[168:171], v[192:195], v[118:121]
	v_mfma_f32_16x16x32_bf16 v[110:113], v[176:179], v[192:195], v[110:113]
	v_mfma_f32_16x16x32_bf16 v[102:105], v[168:171], v[200:203], v[102:105]
	v_mfma_f32_16x16x32_bf16 v[94:97], v[176:179], v[200:203], v[94:97]
	v_mfma_f32_16x16x32_bf16 v[86:89], v[168:171], v[208:211], v[86:89]
	v_mfma_f32_16x16x32_bf16 v[78:81], v[176:179], v[208:211], v[78:81]
	s_nop 0
	s_barrier
	s_add_i32 s21, 0, 0x1c000
	s_add_i32 s20, s20, s29
	v_add_u32_e32 v145, s21, v154
	v_lshl_add_u64 v[160:161], v[160:161], 0, s[6:7]
	s_mov_b32 m0, s20
	ds_read_b128 v[212:215], v145
	ds_read_b128 v[216:219], v145 offset:1024
	ds_read_b128 v[220:223], v145 offset:2048
	ds_read_b128 v[224:227], v145 offset:3072
	global_load_lds_dwordx4 v[160:161], off
	v_lshl_add_u64 v[160:161], v[228:229], 0, s[6:7]
	s_add_i32 m0, s20, 0x2000
	s_nop 0
	global_load_lds_dwordx4 v[160:161], off
	s_barrier
; #define PG8_STAGE_B(bufoff, gbase) do { _Pragma("unroll") for (int _i = 0; _i < 2; ++_i) \
;         __builtin_amdgcn_global_load_lds((const unsigned*)((const char*)(gbase) + voffB[_i]), (LAS unsigned*)(lds + (bufoff) + ldsw + _i * 8192), 16, 0, 0); } while (0)
; #define PG8_STAGE_A(bufoff, AO, h, kb) do { _Pragma("unroll") for (int _i = 0; _i < 2; ++_i) \
;         __builtin_amdgcn_global_load_lds((const unsigned*)(S.A + (size_t)(AO)[h][_i] + (size_t)(kb)), (LAS unsigned*)(lds + (bufoff) + ldsw + _i * 8192), 16, 0, 0); } while (0)
; #define PG8_LDA(dst, b, h) do { _Pragma("unroll") for (int m = 0; m < 4; ++m) { dst[m].lo = *(const LAS i32x4*)(lds + PG8_SA(b, h) + aoff + m * 2048); dst[m].hi = *(const LAS i32x4*)(lds + PG8_SA(b, h) + aoff + m * 2048 + 1024); } } while (0)
; #define PG8_LDB(dst, b, h) do { _Pragma("unroll") for (int n = 0; n < 2; ++n) { dst[n].lo = *(const LAS i32x4*)(lds + PG8_SB(b, h) + boff + n * 2048); dst[n].hi = *(const LAS i32x4*)(lds + PG8_SB(b, h) + boff + n * 2048 + 1024); } } while (0)
; #define PG8_WAIT_V(n) asm volatile("s_waitcnt vmcnt(" #n ")" ::: "memory")
; #define PG8_WAIT_L(n) asm volatile("s_waitcnt lgkmcnt(" #n ")" ::: "memory")
; #define PG8_BAR __builtin_amdgcn_s_barrier()
; #define PG8_SCHED __builtin_amdgcn_sched_barrier(0)
; template <class P>
; __device__ __forceinline__ void gemm_phase(LAS unsigned char* lds, const P& S) {
;     ...
;             PG8_LDB(B0, 1, 0); PG8_SCHED; PG8_LDA(At, 1, 0); PG8_STAGE_A(PG8_SA(0, 1), a2, 1, 0);
;             PG8_WAIT_L(8); PG8_BAR; PG8_WAIT_L(0); PG8_MMA(0, 0, At, B0); PG8_BAR; PG8_SCHED;
;             PG8_LDB(B1, 1, 1); PG8_STAGE_B(PG8_SB(1, 0), b20 + kstepB);
;             PG8_BAR; PG8_WAIT_L(0); PG8_MMA(0, 1, At, B1); PG8_BAR;
;             PG8_LDA(At, 1, 1); PG8_STAGE_A(PG8_SA(1, 0), a2, 0, kstep);
;             PG8_BAR; PG8_WAIT_L(0); PG8_MMA(1, 0, At, B0); PG8_BAR; PG8_SCHED;
;             PG8_STAGE_B(PG8_SB(1, 1), b21 + kstepB);
;             PG8_WAIT_V(6); PG8_BAR; PG8_MMA(1, 1, At, B1); PG8_BAR;
	s_waitcnt lgkmcnt(0)
	s_nop 0
	s_waitcnt lgkmcnt(0)
	v_mfma_f32_16x16x32_bf16 v[114:117], v[212:215], v[180:183], v[114:117]
	v_mfma_f32_16x16x32_bf16 v[106:109], v[220:223], v[180:183], v[106:109]
	v_mfma_f32_16x16x32_bf16 v[98:101], v[212:215], v[188:191], v[98:101]
	v_mfma_f32_16x16x32_bf16 v[90:93], v[220:223], v[188:191], v[90:93]
	v_mfma_f32_16x16x32_bf16 v[82:85], v[212:215], v[196:199], v[82:85]
	v_mfma_f32_16x16x32_bf16 v[74:77], v[220:223], v[196:199], v[74:77]
	v_mfma_f32_16x16x32_bf16 v[70:73], v[212:215], v[204:207], v[70:73]
	v_mfma_f32_16x16x32_bf16 v[66:69], v[220:223], v[204:207], v[66:69]
	v_mfma_f32_16x16x32_bf16 v[114:117], v[216:219], v[184:187], v[114:117]
	v_mfma_f32_16x16x32_bf16 v[106:109], v[224:227], v[184:187], v[106:109]
	v_mfma_f32_16x16x32_bf16 v[98:101], v[216:219], v[192:195], v[98:101]
	v_mfma_f32_16x16x32_bf16 v[90:93], v[224:227], v[192:195], v[90:93]
	v_mfma_f32_16x16x32_bf16 v[82:85], v[216:219], v[200:203], v[82:85]
	v_mfma_f32_16x16x32_bf16 v[74:77], v[224:227], v[200:203], v[74:77]
	v_mfma_f32_16x16x32_bf16 v[70:73], v[216:219], v[208:211], v[70:73]
	v_mfma_f32_16x16x32_bf16 v[66:69], v[224:227], v[208:211], v[66:69]
	s_nop 0
	s_mov_b32 m0, s38
	v_lshl_add_u64 v[160:161], v[230:231], 0, s[6:7]
	s_barrier
	ds_read_b128 v[180:183], v156 offset:49152
	ds_read_b128 v[184:187], v156 offset:50176
	ds_read_b128 v[188:191], v156 offset:51200
	ds_read_b128 v[192:195], v156 offset:52224
	ds_read_b128 v[196:199], v156 offset:53248
	ds_read_b128 v[200:203], v156 offset:54272
	ds_read_b128 v[204:207], v156 offset:55296
	ds_read_b128 v[208:211], v156 offset:56320
	global_load_lds_dwordx4 v[160:161], off
	v_lshl_add_u64 v[160:161], v[232:233], 0, s[6:7]
	s_mov_b32 m0, s39
	s_nop 0
	global_load_lds_dwordx4 v[160:161], off
	s_barrier
	s_waitcnt lgkmcnt(0)
	s_nop 0
	s_waitcnt lgkmcnt(0)
	v_mfma_f32_16x16x32_bf16 v[62:65], v[164:167], v[180:183], v[62:65]
	v_mfma_f32_16x16x32_bf16 v[58:61], v[172:175], v[180:183], v[58:61]
	v_mfma_f32_16x16x32_bf16 v[54:57], v[164:167], v[188:191], v[54:57]
	v_mfma_f32_16x16x32_bf16 v[50:53], v[172:175], v[188:191], v[50:53]
	v_mfma_f32_16x16x32_bf16 v[38:41], v[164:167], v[196:199], v[38:41]
	v_mfma_f32_16x16x32_bf16 v[34:37], v[172:175], v[196:199], v[34:37]
	v_mfma_f32_16x16x32_bf16 v[22:25], v[164:167], v[204:207], v[22:25]
	v_mfma_f32_16x16x32_bf16 v[18:21], v[172:175], v[204:207], v[18:21]
	v_mfma_f32_16x16x32_bf16 v[62:65], v[168:171], v[184:187], v[62:65]
	v_mfma_f32_16x16x32_bf16 v[58:61], v[176:179], v[184:187], v[58:61]
	v_mfma_f32_16x16x32_bf16 v[54:57], v[168:171], v[192:195], v[54:57]
	v_mfma_f32_16x16x32_bf16 v[50:53], v[176:179], v[192:195], v[50:53]
	v_mfma_f32_16x16x32_bf16 v[38:41], v[168:171], v[200:203], v[38:41]
	v_mfma_f32_16x16x32_bf16 v[34:37], v[176:179], v[200:203], v[34:37]
	v_mfma_f32_16x16x32_bf16 v[22:25], v[168:171], v[208:211], v[22:25]
	v_mfma_f32_16x16x32_bf16 v[18:21], v[176:179], v[208:211], v[18:21]
	s_nop 0
	s_barrier
	s_add_i32 s20, s21, s29
	v_lshl_add_u64 v[160:161], v[234:235], 0, s[6:7]
	s_mov_b32 m0, s20
	s_nop 0
	global_load_lds_dwordx4 v[160:161], off
	v_lshl_add_u64 v[160:161], v[236:237], 0, s[6:7]
	s_add_i32 m0, s20, 0x2000
	s_nop 0
	global_load_lds_dwordx4 v[160:161], off
	s_waitcnt vmcnt(6)
	s_barrier
	s_nop 0
	v_mfma_f32_16x16x32_bf16 v[46:49], v[212:215], v[180:183], v[46:49]
	v_mfma_f32_16x16x32_bf16 v[42:45], v[220:223], v[180:183], v[42:45]
	v_mfma_f32_16x16x32_bf16 v[30:33], v[212:215], v[188:191], v[30:33]
	v_mfma_f32_16x16x32_bf16 v[26:29], v[220:223], v[188:191], v[26:29]
	v_mfma_f32_16x16x32_bf16 v[14:17], v[212:215], v[196:199], v[14:17]
	v_mfma_f32_16x16x32_bf16 v[10:13], v[220:223], v[196:199], v[10:13]
	v_mfma_f32_16x16x32_bf16 v[6:9], v[212:215], v[204:207], v[6:9]
	v_mfma_f32_16x16x32_bf16 v[2:5], v[220:223], v[204:207], v[2:5]
	v_mfma_f32_16x16x32_bf16 v[46:49], v[216:219], v[184:187], v[46:49]
	v_mfma_f32_16x16x32_bf16 v[42:45], v[224:227], v[184:187], v[42:45]
	v_mfma_f32_16x16x32_bf16 v[30:33], v[216:219], v[192:195], v[30:33]
	v_mfma_f32_16x16x32_bf16 v[26:29], v[224:227], v[192:195], v[26:29]
	v_mfma_f32_16x16x32_bf16 v[14:17], v[216:219], v[200:203], v[14:17]
	v_mfma_f32_16x16x32_bf16 v[10:13], v[224:227], v[200:203], v[10:13]
	v_mfma_f32_16x16x32_bf16 v[6:9], v[216:219], v[208:211], v[6:9]
	v_mfma_f32_16x16x32_bf16 v[2:5], v[224:227], v[208:211], v[2:5]
	s_nop 0
	s_add_i32 s53, s53, 2
	s_cmp_gt_u32 s53, 29
	s_mov_b64 s[20:21], s[18:19]
	s_barrier
	s_cbranch_scc1 .LBB0_212

; #define PG8_WAIT_V(n) asm volatile("s_waitcnt vmcnt(" #n ")" ::: "memory")
; #define PG8_BAR __builtin_amdgcn_s_barrier()
; template <class P>
; __device__ __forceinline__ void gemm_phase(LAS unsigned char* lds, const P& S) {
;     ...
;     PG8_WAIT_V(0);
;     if (wr == 0) PG8_BAR;
;     PG8_BAR;
.LBB0_226:
	s_setprio 0
	s_barrier

; #define PG8_STAGE_B(bufoff, gbase) do { _Pragma("unroll") for (int _i = 0; _i < 2; ++_i) \
;         __builtin_amdgcn_global_load_lds((const unsigned*)((const char*)(gbase) + voffB[_i]), (LAS unsigned*)(lds + (bufoff) + ldsw + _i * 8192), 16, 0, 0); } while (0)
; #define PG8_WAIT_V(n) asm volatile("s_waitcnt vmcnt(" #n ")" ::: "memory")
; #define PG8_BAR __builtin_amdgcn_s_barrier()
; template <class P>
; __device__ __forceinline__ void gemm_phase(LAS unsigned char* lds, const P& S) {
;     int tid = threadIdx.x; asm volatile("" : "+v"(tid));
;     const int wid = __builtin_amdgcn_readfirstlane(tid >> 6), lane = tid & 63, wr = wid >> 2, wc = wid & 3, fr = lane & 15, fq = lane >> 4;
;     const int K = S.K, nt = K / BK;
;     unsigned voffB[2]; int RA[2], CA[2];
; #pragma unroll
;     for (int i = 0; i < 2; ++i) { int R, C; stage_rc(tid * 16 + i * 8192, R, C); const int Rb = P::PERM ? ((R & ~31) + perm32(R & 31)) : R;
;         RA[i] = R; CA[i] = C; if constexpr (P::BBLK) voffB[i] = (unsigned)((C >> 3) * S.NB + Rb) * 16u; else voffB[i] = (unsigned)(Rb * K + C) * 2u; }
;     const size_t kstep = (size_t)(BK * 2);
;     size_t kstepB = kstep; if constexpr (P::BBLK) kstepB = (size_t)128 * (size_t)S.NB;
;     const unsigned ldsw = (unsigned)wid * 1024u;
;     const int aoff = lds_byte(wr * 64 + fr, fq * 8), boff = lds_byte(wc * 32 + fr, fq * 8);
;     ...
; typedef int i32x2 __attribute__((ext_vector_type(2)));
;     ...
;     Unit cur, nxt; int ui = 0;
;     if (!S.next(0, cur)) return;
;     f32x4 acc[2][2][4][2];
; #pragma unroll
;     for (int a = 0; a < 2; ++a)
; #pragma unroll
;         for (int b = 0; b < 2; ++b)
; #pragma unroll
;             for (int m = 0; m < 4; ++m)
; #pragma unroll
;                 for (int n = 0; n < 2; ++n) acc[a][b][m][n] = (f32x4){0.f, 0.f, 0.f, 0.f};
;     i32x8 At[4], B0[2], B1[2];
;     unsigned ac[2][2], a2[2][2];
;     PG8_AOFF(ac, cur, 0);
;     const char* cB0 = S.bptr(cur, 0); const char* cB1 = S.bptr(cur, 1);
;     PG8_STAGE_B(PG8_SB(0, 0), cB0); PG8_STAGE_A(PG8_SA(0, 0), ac, 0, 0); PG8_STAGE_B(PG8_SB(0, 1), cB1); PG8_STAGE_A(PG8_SA(0, 1), ac, 1, 0);
;     if (wr == 1) PG8_BAR;
;     PG8_WAIT_V(4); PG8_BAR;
;     PG8_STAGE_B(PG8_SB(1, 0), cB0 + kstepB); PG8_STAGE_A(PG8_SA(1, 0), ac, 0, kstep); PG8_STAGE_B(PG8_SB(1, 1), cB1 + kstepB);
;     PG8_WAIT_V(6); PG8_BAR;
.LBB0_846:
	s_cmp_lt_i32 s68, 8
	s_cselect_b64 s[0:1], -1, 0
	s_and_b64 s[2:3], s[0:1], s[4:5]
	s_andn2_b64 vcc, exec, s[2:3]
	s_cbranch_vccnz .LBB0_867
	s_waitcnt vmcnt(0)
	v_mov_b32_e32 v14, v0
	s_cmpk_gt_i32 s80, 0x1ff
	s_nop 0
	v_readfirstlane_b32 s19, v14
	s_cbranch_scc1 .LBB0_867
	v_ashrrev_i32_e32 v1, 31, v14
	v_lshrrev_b32_e32 v1, 26, v1
	v_add_u32_e32 v1, v14, v1
	v_ashrrev_i32_e32 v3, 6, v1
	v_bfe_i32 v1, v14, 27, 1
	v_lshlrev_b32_e32 v2, 4, v14
	v_lshrrev_b32_e32 v1, 22, v1
	v_add_u32_e32 v1, v2, v1
	v_and_b32_e32 v1, 0xfffffc00, v1
	v_sub_u32_e32 v1, v2, v1
	v_add_u32_e32 v2, 0x2000, v2
	v_ashrrev_i32_e32 v7, 31, v2
	v_lshrrev_b32_e32 v7, 22, v7
	v_add_u32_e32 v7, v2, v7
	v_ashrrev_i32_e32 v7, 10, v7
	v_mul_i32_i24_e32 v8, 0x400, v7
	v_sub_u32_e32 v2, v2, v8
	v_lshrrev_b32_e32 v8, 4, v2
	v_bitop3_b32 v2, v8, v2, 32 bitop3:0x6c
	v_ashrrev_i32_e32 v9, 31, v2
	v_lshrrev_b32_e32 v9, 26, v9
	v_lshrrev_b32_e32 v4, 4, v1
	v_lshlrev_b32_e32 v8, 3, v7
	v_add_u32_e32 v9, v2, v9
	v_bitop3_b32 v4, v4, v1, 32 bitop3:0x6c
	v_and_b32_e32 v8, -16, v8
	v_ashrrev_i32_e32 v10, 6, v9
	v_ashrrev_i32_e32 v5, 31, v4
	v_add_u32_e32 v200, v10, v8
	v_and_b32_e32 v8, 0xc0, v9
	v_lshrrev_b32_e32 v5, 26, v5
	v_sub_u32_e32 v2, v2, v8
	v_mov_b32_e32 v8, 1
	s_waitcnt lgkmcnt(0)
	s_add_u32 s2, s86, 0x5d000000
	v_lshlrev_b32_e32 v1, 3, v3
	v_add_u32_e32 v5, v4, v5
	v_lshlrev_b32_e32 v7, 5, v7
	v_ashrrev_i16_sdwa v2, v8, sext(v2) dst_sel:DWORD dst_unused:UNUSED_PAD src0_sel:DWORD src1_sel:BYTE_0
	s_addc_u32 s3, s87, 0
	v_and_b32_e32 v1, -16, v1
	v_ashrrev_i32_e32 v6, 6, v5
	v_and_b32_e32 v7, 32, v7
	v_bfe_i32 v2, v2, 0, 16
	v_and_b32_e32 v5, 0xc0, v5
	s_add_u32 s33, s86, 0x2600000
	v_add_u32_e32 v1, v6, v1
	v_sub_u32_e32 v4, v4, v5
	v_and_b32_e32 v5, 3, v10
	s_mov_b32 s4, 0xfffe0
	v_add_lshl_u32 v201, v7, v2, 1
	v_and_b32_e32 v2, 3, v6
	s_addc_u32 s38, s87, 0
	v_and_or_b32 v5, v200, s4, v5
	v_and_or_b32 v2, v1, s4, v2
	s_ashr_i32 s4, s80, 31
	s_lshr_b32 s4, s4, 29
	s_add_i32 s4, s80, s4
	s_ashr_i32 s5, s4, 3
	s_and_b32 s4, s4, -8
	s_ashr_i32 s17, s19, 6
	s_sub_i32 s4, s80, s4
	s_ashr_i32 s16, s19, 8
	s_lshl_b32 s39, s17, 10
	s_lshl_b32 s7, s4, 6
	s_mul_i32 s6, s4, 0x41
	s_cmp_lt_i32 s4, 0
	s_cselect_b32 s4, s6, s7
	s_add_i32 s4, s4, s5
	s_ashr_i32 s5, s4, 31
	s_lshr_b32 s5, s5, 26
	s_add_i32 s5, s4, s5
	s_ashr_i32 s6, s5, 6
	s_andn2_b32 s5, s5, 63
	s_sub_i32 s4, s4, s5
	s_bfe_i32 s5, s4, 0x80000
	s_bfe_u32 s5, s5, 0x3000c
	v_ashrrev_i16_sdwa v4, v8, sext(v4) dst_sel:DWORD dst_unused:UNUSED_PAD src0_sel:DWORD src1_sel:BYTE_0
	v_lshrrev_b32_e32 v8, 2, v200
	v_lshlrev_b32_e32 v9, 1, v200
	s_add_i32 s5, s4, s5
	v_and_b32_e32 v8, 4, v8
	v_and_b32_e32 v9, 24, v9
	s_bfe_i32 s7, s5, 0x80000
	s_and_b32 s5, s5, 0xf8
	v_or3_b32 v5, v5, v8, v9
	s_sub_i32 s4, s4, s5
	v_lshlrev_b32_e32 v3, 5, v3
	v_lshl_add_u32 v154, v5, 12, v201
	v_lshrrev_b32_e32 v5, 2, v1
	v_lshlrev_b32_e32 v6, 1, v1
	s_lshl_b32 s6, s6, 3
	s_sext_i32_i8 s4, s4
	v_and_b32_e32 v3, 32, v3
	v_bfe_i32 v4, v4, 0, 16
	v_and_b32_e32 v5, 4, v5
	v_and_b32_e32 v6, 24, v6
	s_add_i32 s51, s6, s4
	v_or3_b32 v2, v2, v5, v6
	v_add_lshl_u32 v209, v3, v4, 1
	s_lshl_b32 s4, s51, 8
	v_lshl_add_u32 v156, v2, 12, v209
	v_add_u32_e32 v2, s4, v1
	s_sext_i32_i16 s7, s7
	v_lshl_add_u32 v130, v2, 12, v209
	v_add_u32_e32 v2, s4, v200
	s_bitset1_b32 s4, 7
	s_ashr_i32 s52, s7, 3
	v_lshl_add_u32 v132, v2, 12, v201
	v_add_u32_e32 v2, s4, v1
	v_lshl_add_u32 v134, v2, 12, v209
	v_add_u32_e32 v2, s4, v200
	s_lshl_b32 s4, s52, 8
	s_ashr_i32 s5, s4, 31
	s_lshl_b64 s[6:7], s[4:5], 12
	s_add_u32 s28, s33, s6
	s_addc_u32 s29, s38, s7
	s_add_i32 s40, s39, 0
	s_bitset1_b32 s4, 7
	s_add_i32 m0, s40, 0x10000
	s_ashr_i32 s5, s4, 31
	global_load_lds_dwordx4 v156, s[28:29]
	s_add_i32 m0, s40, 0x12000
	s_lshl_b64 s[4:5], s[4:5], 12
	global_load_lds_dwordx4 v154, s[28:29]
	s_mov_b32 m0, s40
	s_add_i32 s41, s40, 0x2000
	global_load_lds_dwordx4 v130, s[2:3]
	s_mov_b32 m0, s41
	s_add_u32 s30, s33, s4
	global_load_lds_dwordx4 v132, s[2:3]
	s_addc_u32 s31, s38, s5
	s_add_i32 m0, s40, 0x14000
	s_add_i32 s42, s40, 0x4000
	global_load_lds_dwordx4 v156, s[30:31]
	s_add_i32 m0, s40, 0x16000
	s_add_i32 s43, s40, 0x6000
	global_load_lds_dwordx4 v154, s[30:31]
	s_mov_b32 m0, s42
	v_lshl_add_u32 v136, v2, 12, v201
	global_load_lds_dwordx4 v134, s[2:3]
	s_mov_b32 m0, s43
	s_load_dwordx4 s[4:7], s[88:89], 0x20
	global_load_lds_dwordx4 v136, s[2:3]
	v_mov_b32_e32 v159, 0
	v_mov_b32_e32 v157, v159
	v_mov_b32_e32 v155, v159
	v_mov_b32_e32 v131, v159
	v_mov_b32_e32 v133, v159
	s_mov_b32 s44, 0
	v_lshl_add_u64 v[12:13], s[28:29], 0, v[156:157]
	v_lshl_add_u64 v[10:11], s[28:29], 0, v[154:155]
	v_lshl_add_u64 v[8:9], s[2:3], 0, v[130:131]
	v_lshl_add_u64 v[6:7], s[2:3], 0, v[132:133]
	v_lshl_add_u64 v[4:5], s[30:31], 0, v[156:157]
	s_cmp_lg_u32 s16, 1
	v_lshl_add_u64 v[2:3], s[30:31], 0, v[154:155]
	s_cbranch_scc1 .LBB0_850
	s_setprio 1
	s_barrier

; #define PG8_STAGE_B(bufoff, gbase) do { _Pragma("unroll") for (int _i = 0; _i < 2; ++_i) \
;         __builtin_amdgcn_global_load_lds((const unsigned*)((const char*)(gbase) + voffB[_i]), (LAS unsigned*)(lds + (bufoff) + ldsw + _i * 8192), 16, 0, 0); } while (0)
; #define PG8_STAGE_A(bufoff, AO, h, kb) do { _Pragma("unroll") for (int _i = 0; _i < 2; ++_i) \
;         __builtin_amdgcn_global_load_lds((const unsigned*)(S.A + (size_t)(AO)[h][_i] + (size_t)(kb)), (LAS unsigned*)(lds + (bufoff) + ldsw + _i * 8192), 16, 0, 0); } while (0)
; #define PG8_LDA(dst, b, h) do { _Pragma("unroll") for (int m = 0; m < 4; ++m) { dst[m].lo = *(const LAS i32x4*)(lds + PG8_SA(b, h) + aoff + m * 2048); dst[m].hi = *(const LAS i32x4*)(lds + PG8_SA(b, h) + aoff + m * 2048 + 1024); } } while (0)
; #define PG8_LDB(dst, b, h) do { _Pragma("unroll") for (int n = 0; n < 2; ++n) { dst[n].lo = *(const LAS i32x4*)(lds + PG8_SB(b, h) + boff + n * 2048); dst[n].hi = *(const LAS i32x4*)(lds + PG8_SB(b, h) + boff + n * 2048 + 1024); } } while (0)
; #define PG8_WAIT_V(n) asm volatile("s_waitcnt vmcnt(" #n ")" ::: "memory")
; #define PG8_WAIT_L(n) asm volatile("s_waitcnt lgkmcnt(" #n ")" ::: "memory")
; template <class P>
; __device__ __forceinline__ void gemm_phase(LAS unsigned char* lds, const P& S) {
;     ...
;             PG8_LDB(B0, 0, 0); PG8_SCHED; PG8_LDA(At, 0, 0); PG8_STAGE_A(PG8_SA(1, 1), ac, 1, k1);
;             PG8_WAIT_L(8); PG8_BAR; PG8_WAIT_L(0); PG8_MMA(0, 0, At, B0); PG8_BAR; PG8_SCHED;
;             PG8_LDB(B1, 0, 1); PG8_STAGE_B(PG8_SB(0, 0), b20);
;             PG8_BAR; PG8_WAIT_L(0); PG8_MMA(0, 1, At, B1); PG8_BAR;
;             PG8_LDA(At, 0, 1); PG8_STAGE_A(PG8_SA(0, 0), a2, 0, 0);
;             PG8_BAR; PG8_WAIT_L(0); PG8_MMA(1, 0, At, B0); PG8_BAR; PG8_SCHED;
;             PG8_STAGE_B(PG8_SB(0, 1), b21);
;             PG8_WAIT_V(6); PG8_BAR; PG8_MMA(1, 1, At, B1); PG8_BAR;
;             PG8_LDB(B0, 1, 0); PG8_SCHED; PG8_LDA(At, 1, 0); PG8_STAGE_A(PG8_SA(0, 1), a2, 1, 0);
;             PG8_WAIT_L(8); PG8_BAR; PG8_WAIT_L(0); PG8_MMA(0, 0, At, B0); PG8_BAR; PG8_SCHED;
;             PG8_LDB(B1, 1, 1); PG8_STAGE_B(PG8_SB(1, 0), b20 + kstepB);
;             PG8_BAR; PG8_WAIT_L(0); PG8_MMA(0, 1, At, B1); PG8_BAR;
;             PG8_LDA(At, 1, 1); PG8_STAGE_A(PG8_SA(1, 0), a2, 0, kstep);
;             PG8_BAR; PG8_WAIT_L(0); PG8_MMA(1, 0, At, B0); PG8_BAR; PG8_SCHED;
.LBB0_859:
	v_add_u32_e32 v135, s47, v204
	ds_read_b128 v[144:147], v135
	ds_read_b128 v[148:151], v135 offset:1024
	ds_read_b128 v[162:165], v135 offset:2048
	ds_read_b128 v[166:169], v135 offset:3072
	s_add_u32 s60, s55, s30
	s_addc_u32 s61, s56, s31
	s_add_u32 s62, s57, s30
	s_addc_u32 s63, s58, s31
	s_and_b64 s[36:37], s[34:35], exec
	s_cselect_b32 s37, s53, s61
	s_cselect_b32 s36, s54, s60
	v_lshl_add_u64 v[152:153], v[138:139], 0, s[30:31]
	s_add_i32 m0, s40, 0xc000
	ds_read_b128 v[170:173], v206
	ds_read_b128 v[174:177], v206 offset:1024
	ds_read_b128 v[178:181], v206 offset:2048
	ds_read_b128 v[182:185], v206 offset:3072
	ds_read_b128 v[186:189], v206 offset:4096
	ds_read_b128 v[190:193], v206 offset:5120
	ds_read_b128 v[194:197], v206 offset:6144
	ds_read_b128 v[210:213], v206 offset:7168
	global_load_lds_dwordx4 v[152:153], off
	v_lshl_add_u64 v[152:153], v[140:141], 0, s[30:31]
	s_add_i32 m0, s40, 0xe000
	s_nop 0
	global_load_lds_dwordx4 v[152:153], off
	s_waitcnt lgkmcnt(8)
	s_barrier
	s_waitcnt lgkmcnt(0)
	s_nop 0
	s_waitcnt lgkmcnt(0)
	v_mfma_f32_16x16x32_bf16 v[126:129], v[144:147], v[170:173], v[126:129]
	v_mfma_f32_16x16x32_bf16 v[122:125], v[162:165], v[170:173], v[122:125]
	v_mfma_f32_16x16x32_bf16 v[118:121], v[144:147], v[178:181], v[118:121]
	v_mfma_f32_16x16x32_bf16 v[114:117], v[162:165], v[178:181], v[114:117]
	v_mfma_f32_16x16x32_bf16 v[110:113], v[144:147], v[186:189], v[110:113]
	v_mfma_f32_16x16x32_bf16 v[106:109], v[162:165], v[186:189], v[106:109]
	v_mfma_f32_16x16x32_bf16 v[102:105], v[144:147], v[194:197], v[102:105]
	v_mfma_f32_16x16x32_bf16 v[98:101], v[162:165], v[194:197], v[98:101]
	v_mfma_f32_16x16x32_bf16 v[126:129], v[148:151], v[174:177], v[126:129]
	v_mfma_f32_16x16x32_bf16 v[122:125], v[166:169], v[174:177], v[122:125]
	v_mfma_f32_16x16x32_bf16 v[118:121], v[148:151], v[182:185], v[118:121]
	v_mfma_f32_16x16x32_bf16 v[114:117], v[166:169], v[182:185], v[114:117]
	v_mfma_f32_16x16x32_bf16 v[110:113], v[148:151], v[190:193], v[110:113]
	v_mfma_f32_16x16x32_bf16 v[106:109], v[166:169], v[190:193], v[106:109]
	v_mfma_f32_16x16x32_bf16 v[102:105], v[148:151], v[210:213], v[102:105]
	v_mfma_f32_16x16x32_bf16 v[98:101], v[166:169], v[210:213], v[98:101]
	s_nop 0
	s_barrier
	s_add_i32 s30, s47, s39
	v_add_u32_e32 v135, s48, v204
	v_lshl_add_u64 v[152:153], s[36:37], 0, v[156:157]
	s_mov_b32 m0, s30
	ds_read_b128 v[214:217], v135
	ds_read_b128 v[218:221], v135 offset:1024
	ds_read_b128 v[222:225], v135 offset:2048
	ds_read_b128 v[226:229], v135 offset:3072
	global_load_lds_dwordx4 v[152:153], off
	v_lshl_add_u64 v[198:199], s[36:37], 0, v[154:155]
	s_add_i32 m0, s30, 0x2000
	s_nop 0
	global_load_lds_dwordx4 v[198:199], off
	s_barrier
	s_waitcnt lgkmcnt(0)
	s_nop 0
	s_waitcnt lgkmcnt(0)
	v_mfma_f32_16x16x32_bf16 v[66:69], v[214:217], v[170:173], v[66:69]
	v_mfma_f32_16x16x32_bf16 v[58:61], v[222:225], v[170:173], v[58:61]
	v_mfma_f32_16x16x32_bf16 v[54:57], v[214:217], v[178:181], v[54:57]
	v_mfma_f32_16x16x32_bf16 v[50:53], v[222:225], v[178:181], v[50:53]
	v_mfma_f32_16x16x32_bf16 v[46:49], v[214:217], v[186:189], v[46:49]
	v_mfma_f32_16x16x32_bf16 v[42:45], v[222:225], v[186:189], v[42:45]
	v_mfma_f32_16x16x32_bf16 v[38:41], v[214:217], v[194:197], v[38:41]
	v_mfma_f32_16x16x32_bf16 v[34:37], v[222:225], v[194:197], v[34:37]
	v_mfma_f32_16x16x32_bf16 v[66:69], v[218:221], v[174:177], v[66:69]
	v_mfma_f32_16x16x32_bf16 v[58:61], v[226:229], v[174:177], v[58:61]
	v_mfma_f32_16x16x32_bf16 v[54:57], v[218:221], v[182:185], v[54:57]
	v_mfma_f32_16x16x32_bf16 v[50:53], v[226:229], v[182:185], v[50:53]
	v_mfma_f32_16x16x32_bf16 v[46:49], v[218:221], v[190:193], v[46:49]
	v_mfma_f32_16x16x32_bf16 v[42:45], v[226:229], v[190:193], v[42:45]
	v_mfma_f32_16x16x32_bf16 v[38:41], v[218:221], v[210:213], v[38:41]
	v_mfma_f32_16x16x32_bf16 v[34:37], v[226:229], v[210:213], v[34:37]
	s_nop 0
	s_mov_b32 m0, s40
	s_barrier
	ds_read_b128 v[170:173], v206 offset:16384
	ds_read_b128 v[174:177], v206 offset:17408
	ds_read_b128 v[178:181], v206 offset:18432
	ds_read_b128 v[182:185], v206 offset:19456
	ds_read_b128 v[186:189], v206 offset:20480
	ds_read_b128 v[190:193], v206 offset:21504
	ds_read_b128 v[194:197], v206 offset:22528
	ds_read_b128 v[210:213], v206 offset:23552
	global_load_lds_dwordx4 v158, s[2:3]
	s_mov_b32 m0, s41
	v_mov_b32_e32 v161, v159
	global_load_lds_dwordx4 v160, s[2:3]
	s_barrier
	s_waitcnt lgkmcnt(0)
	v_lshl_add_u64 v[202:203], s[2:3], 0, v[158:159]
	v_lshl_add_u64 v[230:231], s[2:3], 0, v[160:161]
	s_nop 0
	s_waitcnt lgkmcnt(0)
	v_mfma_f32_16x16x32_bf16 v[94:97], v[144:147], v[170:173], v[94:97]
	s_and_b64 s[30:31], s[34:35], exec
	s_cselect_b32 s31, s25, s63
	s_cselect_b32 s30, s24, s62
	v_mfma_f32_16x16x32_bf16 v[90:93], v[162:165], v[170:173], v[90:93]
	v_mfma_f32_16x16x32_bf16 v[86:89], v[144:147], v[178:181], v[86:89]
	v_mfma_f32_16x16x32_bf16 v[82:85], v[162:165], v[178:181], v[82:85]
	v_mfma_f32_16x16x32_bf16 v[78:81], v[144:147], v[186:189], v[78:81]
	v_mfma_f32_16x16x32_bf16 v[74:77], v[162:165], v[186:189], v[74:77]
	v_mfma_f32_16x16x32_bf16 v[70:73], v[144:147], v[194:197], v[70:73]
	v_mfma_f32_16x16x32_bf16 v[62:65], v[162:165], v[194:197], v[62:65]
	v_mfma_f32_16x16x32_bf16 v[94:97], v[148:151], v[174:177], v[94:97]
	v_mfma_f32_16x16x32_bf16 v[90:93], v[166:169], v[174:177], v[90:93]
	v_mfma_f32_16x16x32_bf16 v[86:89], v[148:151], v[182:185], v[86:89]
	v_mfma_f32_16x16x32_bf16 v[82:85], v[166:169], v[182:185], v[82:85]
	v_mfma_f32_16x16x32_bf16 v[78:81], v[148:151], v[190:193], v[78:81]
	v_mfma_f32_16x16x32_bf16 v[74:77], v[166:169], v[190:193], v[74:77]
	v_mfma_f32_16x16x32_bf16 v[70:73], v[148:151], v[210:213], v[70:73]
	v_mfma_f32_16x16x32_bf16 v[62:65], v[166:169], v[210:213], v[62:65]
	s_nop 0
	s_barrier
; #define PG8_STAGE_B(bufoff, gbase) do { _Pragma("unroll") for (int _i = 0; _i < 2; ++_i) \
;         __builtin_amdgcn_global_load_lds((const unsigned*)((const char*)(gbase) + voffB[_i]), (LAS unsigned*)(lds + (bufoff) + ldsw + _i * 8192), 16, 0, 0); } while (0)
; #define PG8_STAGE_A(bufoff, AO, h, kb) do { _Pragma("unroll") for (int _i = 0; _i < 2; ++_i) \
;         __builtin_amdgcn_global_load_lds((const unsigned*)(S.A + (size_t)(AO)[h][_i] + (size_t)(kb)), (LAS unsigned*)(lds + (bufoff) + ldsw + _i * 8192), 16, 0, 0); } while (0)
; #define PG8_LDA(dst, b, h) do { _Pragma("unroll") for (int m = 0; m < 4; ++m) { dst[m].lo = *(const LAS i32x4*)(lds + PG8_SA(b, h) + aoff + m * 2048); dst[m].hi = *(const LAS i32x4*)(lds + PG8_SA(b, h) + aoff + m * 2048 + 1024); } } while (0)
; #define PG8_LDB(dst, b, h) do { _Pragma("unroll") for (int n = 0; n < 2; ++n) { dst[n].lo = *(const LAS i32x4*)(lds + PG8_SB(b, h) + boff + n * 2048); dst[n].hi = *(const LAS i32x4*)(lds + PG8_SB(b, h) + boff + n * 2048 + 1024); } } while (0)
; #define PG8_WAIT_V(n) asm volatile("s_waitcnt vmcnt(" #n ")" ::: "memory")
; #define PG8_WAIT_L(n) asm volatile("s_waitcnt lgkmcnt(" #n ")" ::: "memory")
; #define PG8_BAR __builtin_amdgcn_s_barrier()
; #define PG8_SCHED __builtin_amdgcn_sched_barrier(0)
; template <class P>
; __device__ __forceinline__ void gemm_phase(LAS unsigned char* lds, const P& S) {
;     ...
;             PG8_STAGE_B(PG8_SB(0, 1), b21);
;             PG8_WAIT_V(6); PG8_BAR; PG8_MMA(1, 1, At, B1); PG8_BAR;
;             PG8_LDB(B0, 1, 0); PG8_SCHED; PG8_LDA(At, 1, 0); PG8_STAGE_A(PG8_SA(0, 1), a2, 1, 0);
;             PG8_WAIT_L(8); PG8_BAR; PG8_WAIT_L(0); PG8_MMA(0, 0, At, B0); PG8_BAR; PG8_SCHED;
;             PG8_LDB(B1, 1, 1); PG8_STAGE_B(PG8_SB(1, 0), b20 + kstepB);
;             PG8_BAR; PG8_WAIT_L(0); PG8_MMA(0, 1, At, B1); PG8_BAR;
;             PG8_LDA(At, 1, 1); PG8_STAGE_A(PG8_SA(1, 0), a2, 0, kstep);
;             PG8_BAR; PG8_WAIT_L(0); PG8_MMA(1, 0, At, B0); PG8_BAR; PG8_SCHED;
;             PG8_STAGE_B(PG8_SB(1, 1), b21 + kstepB);
;             PG8_WAIT_V(6); PG8_BAR; PG8_MMA(1, 1, At, B1); PG8_BAR;
	s_add_i32 s34, s48, s39
	v_lshl_add_u64 v[232:233], s[30:31], 0, v[156:157]
	s_mov_b32 m0, s34
	v_lshl_add_u64 v[234:235], s[30:31], 0, v[154:155]
	global_load_lds_dwordx4 v[232:233], off
	s_add_i32 m0, s34, 0x2000
	s_nop 0
	global_load_lds_dwordx4 v[234:235], off
	s_waitcnt vmcnt(6)
	s_barrier
	s_nop 0
	v_mfma_f32_16x16x32_bf16 v[30:33], v[214:217], v[170:173], v[30:33]
	v_mfma_f32_16x16x32_bf16 v[26:29], v[222:225], v[170:173], v[26:29]
	v_mfma_f32_16x16x32_bf16 v[22:25], v[214:217], v[178:181], v[22:25]
	v_mfma_f32_16x16x32_bf16 v[18:21], v[222:225], v[178:181], v[18:21]
	v_mfma_f32_16x16x32_bf16 v[14:17], v[214:217], v[186:189], v[14:17]
	v_mfma_f32_16x16x32_bf16 v[10:13], v[222:225], v[186:189], v[10:13]
	v_mfma_f32_16x16x32_bf16 v[6:9], v[214:217], v[194:197], v[6:9]
	v_mfma_f32_16x16x32_bf16 v[2:5], v[222:225], v[194:197], v[2:5]
	v_mfma_f32_16x16x32_bf16 v[30:33], v[218:221], v[174:177], v[30:33]
	v_mfma_f32_16x16x32_bf16 v[26:29], v[226:229], v[174:177], v[26:29]
	v_mfma_f32_16x16x32_bf16 v[22:25], v[218:221], v[182:185], v[22:25]
	v_mfma_f32_16x16x32_bf16 v[18:21], v[226:229], v[182:185], v[18:21]
	v_mfma_f32_16x16x32_bf16 v[14:17], v[218:221], v[190:193], v[14:17]
	v_mfma_f32_16x16x32_bf16 v[10:13], v[226:229], v[190:193], v[10:13]
	v_mfma_f32_16x16x32_bf16 v[6:9], v[218:221], v[210:213], v[6:9]
	v_mfma_f32_16x16x32_bf16 v[2:5], v[226:229], v[210:213], v[2:5]
	s_nop 0
	s_add_i32 s30, 0, 0x18000
	v_add_u32_e32 v135, s30, v204
	s_barrier
	ds_read_b128 v[144:147], v135
	ds_read_b128 v[148:151], v135 offset:1024
	ds_read_b128 v[162:165], v135 offset:2048
	ds_read_b128 v[166:169], v135 offset:3072
	s_mov_b32 m0, s42
	ds_read_b128 v[170:173], v206 offset:32768
	ds_read_b128 v[174:177], v206 offset:33792
	ds_read_b128 v[178:181], v206 offset:34816
	ds_read_b128 v[182:185], v206 offset:35840
	ds_read_b128 v[186:189], v206 offset:36864
	ds_read_b128 v[190:193], v206 offset:37888
	ds_read_b128 v[194:197], v206 offset:38912
	ds_read_b128 v[210:213], v206 offset:39936
	global_load_lds_dwordx4 v208, s[2:3]
	s_mov_b32 m0, s43
	s_nop 0
	global_load_lds_dwordx4 v207, s[2:3]
	s_waitcnt lgkmcnt(8)
	s_barrier
	s_waitcnt lgkmcnt(0)
	s_nop 0
	s_waitcnt lgkmcnt(0)
	v_mfma_f32_16x16x32_bf16 v[126:129], v[144:147], v[170:173], v[126:129]
	v_mfma_f32_16x16x32_bf16 v[122:125], v[162:165], v[170:173], v[122:125]
	v_mfma_f32_16x16x32_bf16 v[118:121], v[144:147], v[178:181], v[118:121]
	v_mfma_f32_16x16x32_bf16 v[114:117], v[162:165], v[178:181], v[114:117]
	v_mfma_f32_16x16x32_bf16 v[110:113], v[144:147], v[186:189], v[110:113]
	v_mfma_f32_16x16x32_bf16 v[106:109], v[162:165], v[186:189], v[106:109]
	v_mfma_f32_16x16x32_bf16 v[102:105], v[144:147], v[194:197], v[102:105]
	v_mfma_f32_16x16x32_bf16 v[98:101], v[162:165], v[194:197], v[98:101]
	v_mfma_f32_16x16x32_bf16 v[126:129], v[148:151], v[174:177], v[126:129]
	v_mfma_f32_16x16x32_bf16 v[122:125], v[166:169], v[174:177], v[122:125]
	v_mfma_f32_16x16x32_bf16 v[118:121], v[148:151], v[182:185], v[118:121]
	v_mfma_f32_16x16x32_bf16 v[114:117], v[166:169], v[182:185], v[114:117]
	v_mfma_f32_16x16x32_bf16 v[110:113], v[148:151], v[190:193], v[110:113]
	v_mfma_f32_16x16x32_bf16 v[106:109], v[166:169], v[190:193], v[106:109]
	v_mfma_f32_16x16x32_bf16 v[102:105], v[148:151], v[210:213], v[102:105]
	v_mfma_f32_16x16x32_bf16 v[98:101], v[166:169], v[210:213], v[98:101]
	s_nop 0
	s_barrier
	s_add_i32 s31, 0, 0x1c000
	s_add_i32 s30, s30, s39
	v_add_u32_e32 v135, s31, v204
	v_lshl_add_u64 v[152:153], v[152:153], 0, s[12:13]
	s_mov_b32 m0, s30
	ds_read_b128 v[214:217], v135
	ds_read_b128 v[218:221], v135 offset:1024
	ds_read_b128 v[222:225], v135 offset:2048
	ds_read_b128 v[226:229], v135 offset:3072
	global_load_lds_dwordx4 v[152:153], off
	v_lshl_add_u64 v[152:153], v[198:199], 0, s[12:13]
	s_add_i32 m0, s30, 0x2000
	s_nop 0
	global_load_lds_dwordx4 v[152:153], off
	s_barrier
; #define PG8_STAGE_B(bufoff, gbase) do { _Pragma("unroll") for (int _i = 0; _i < 2; ++_i) \
;         __builtin_amdgcn_global_load_lds((const unsigned*)((const char*)(gbase) + voffB[_i]), (LAS unsigned*)(lds + (bufoff) + ldsw + _i * 8192), 16, 0, 0); } while (0)
; #define PG8_STAGE_A(bufoff, AO, h, kb) do { _Pragma("unroll") for (int _i = 0; _i < 2; ++_i) \
;         __builtin_amdgcn_global_load_lds((const unsigned*)(S.A + (size_t)(AO)[h][_i] + (size_t)(kb)), (LAS unsigned*)(lds + (bufoff) + ldsw + _i * 8192), 16, 0, 0); } while (0)
; #define PG8_LDA(dst, b, h) do { _Pragma("unroll") for (int m = 0; m < 4; ++m) { dst[m].lo = *(const LAS i32x4*)(lds + PG8_SA(b, h) + aoff + m * 2048); dst[m].hi = *(const LAS i32x4*)(lds + PG8_SA(b, h) + aoff + m * 2048 + 1024); } } while (0)
; #define PG8_LDB(dst, b, h) do { _Pragma("unroll") for (int n = 0; n < 2; ++n) { dst[n].lo = *(const LAS i32x4*)(lds + PG8_SB(b, h) + boff + n * 2048); dst[n].hi = *(const LAS i32x4*)(lds + PG8_SB(b, h) + boff + n * 2048 + 1024); } } while (0)
; #define PG8_WAIT_V(n) asm volatile("s_waitcnt vmcnt(" #n ")" ::: "memory")
; #define PG8_WAIT_L(n) asm volatile("s_waitcnt lgkmcnt(" #n ")" ::: "memory")
; #define PG8_BAR __builtin_amdgcn_s_barrier()
; #define PG8_SCHED __builtin_amdgcn_sched_barrier(0)
; template <class P>
; __device__ __forceinline__ void gemm_phase(LAS unsigned char* lds, const P& S) {
;     ...
;             PG8_LDB(B0, 1, 0); PG8_SCHED; PG8_LDA(At, 1, 0); PG8_STAGE_A(PG8_SA(0, 1), a2, 1, 0);
;             PG8_WAIT_L(8); PG8_BAR; PG8_WAIT_L(0); PG8_MMA(0, 0, At, B0); PG8_BAR; PG8_SCHED;
;             PG8_LDB(B1, 1, 1); PG8_STAGE_B(PG8_SB(1, 0), b20 + kstepB);
;             PG8_BAR; PG8_WAIT_L(0); PG8_MMA(0, 1, At, B1); PG8_BAR;
;             PG8_LDA(At, 1, 1); PG8_STAGE_A(PG8_SA(1, 0), a2, 0, kstep);
;             PG8_BAR; PG8_WAIT_L(0); PG8_MMA(1, 0, At, B0); PG8_BAR; PG8_SCHED;
;             PG8_STAGE_B(PG8_SB(1, 1), b21 + kstepB);
;             PG8_WAIT_V(6); PG8_BAR; PG8_MMA(1, 1, At, B1); PG8_BAR;
	s_waitcnt lgkmcnt(0)
	s_nop 0
	s_waitcnt lgkmcnt(0)
	v_mfma_f32_16x16x32_bf16 v[66:69], v[214:217], v[170:173], v[66:69]
	v_mfma_f32_16x16x32_bf16 v[58:61], v[222:225], v[170:173], v[58:61]
	v_mfma_f32_16x16x32_bf16 v[54:57], v[214:217], v[178:181], v[54:57]
	v_mfma_f32_16x16x32_bf16 v[50:53], v[222:225], v[178:181], v[50:53]
	v_mfma_f32_16x16x32_bf16 v[46:49], v[214:217], v[186:189], v[46:49]
	v_mfma_f32_16x16x32_bf16 v[42:45], v[222:225], v[186:189], v[42:45]
	v_mfma_f32_16x16x32_bf16 v[38:41], v[214:217], v[194:197], v[38:41]
	v_mfma_f32_16x16x32_bf16 v[34:37], v[222:225], v[194:197], v[34:37]
	v_mfma_f32_16x16x32_bf16 v[66:69], v[218:221], v[174:177], v[66:69]
	v_mfma_f32_16x16x32_bf16 v[58:61], v[226:229], v[174:177], v[58:61]
	v_mfma_f32_16x16x32_bf16 v[54:57], v[218:221], v[182:185], v[54:57]
	v_mfma_f32_16x16x32_bf16 v[50:53], v[226:229], v[182:185], v[50:53]
	v_mfma_f32_16x16x32_bf16 v[46:49], v[218:221], v[190:193], v[46:49]
	v_mfma_f32_16x16x32_bf16 v[42:45], v[226:229], v[190:193], v[42:45]
	v_mfma_f32_16x16x32_bf16 v[38:41], v[218:221], v[210:213], v[38:41]
	v_mfma_f32_16x16x32_bf16 v[34:37], v[226:229], v[210:213], v[34:37]
	s_nop 0
	s_mov_b32 m0, s45
	v_lshl_add_u64 v[152:153], v[202:203], 0, s[12:13]
	s_barrier
	ds_read_b128 v[170:173], v206 offset:49152
	ds_read_b128 v[174:177], v206 offset:50176
	ds_read_b128 v[178:181], v206 offset:51200
	ds_read_b128 v[182:185], v206 offset:52224
	ds_read_b128 v[186:189], v206 offset:53248
	ds_read_b128 v[190:193], v206 offset:54272
	ds_read_b128 v[194:197], v206 offset:55296
	ds_read_b128 v[210:213], v206 offset:56320
	global_load_lds_dwordx4 v[152:153], off
	v_lshl_add_u64 v[152:153], v[230:231], 0, s[12:13]
	s_mov_b32 m0, s46
	s_nop 0
	global_load_lds_dwordx4 v[152:153], off
	s_barrier
	s_waitcnt lgkmcnt(0)
	s_nop 0
	s_waitcnt lgkmcnt(0)
	v_mfma_f32_16x16x32_bf16 v[94:97], v[144:147], v[170:173], v[94:97]
	v_mfma_f32_16x16x32_bf16 v[90:93], v[162:165], v[170:173], v[90:93]
	v_mfma_f32_16x16x32_bf16 v[86:89], v[144:147], v[178:181], v[86:89]
	v_mfma_f32_16x16x32_bf16 v[82:85], v[162:165], v[178:181], v[82:85]
	v_mfma_f32_16x16x32_bf16 v[78:81], v[144:147], v[186:189], v[78:81]
	v_mfma_f32_16x16x32_bf16 v[74:77], v[162:165], v[186:189], v[74:77]
	v_mfma_f32_16x16x32_bf16 v[70:73], v[144:147], v[194:197], v[70:73]
	v_mfma_f32_16x16x32_bf16 v[62:65], v[162:165], v[194:197], v[62:65]
	v_mfma_f32_16x16x32_bf16 v[94:97], v[148:151], v[174:177], v[94:97]
	v_mfma_f32_16x16x32_bf16 v[90:93], v[166:169], v[174:177], v[90:93]
	v_mfma_f32_16x16x32_bf16 v[86:89], v[148:151], v[182:185], v[86:89]
	v_mfma_f32_16x16x32_bf16 v[82:85], v[166:169], v[182:185], v[82:85]
	v_mfma_f32_16x16x32_bf16 v[78:81], v[148:151], v[190:193], v[78:81]
	v_mfma_f32_16x16x32_bf16 v[74:77], v[166:169], v[190:193], v[74:77]
	v_mfma_f32_16x16x32_bf16 v[70:73], v[148:151], v[210:213], v[70:73]
	v_mfma_f32_16x16x32_bf16 v[62:65], v[166:169], v[210:213], v[62:65]
	s_nop 0
	s_barrier
	s_add_i32 s30, s31, s39
	v_lshl_add_u64 v[144:145], v[232:233], 0, s[12:13]
	s_mov_b32 m0, s30
	s_nop 0
	global_load_lds_dwordx4 v[144:145], off
	v_lshl_add_u64 v[144:145], v[234:235], 0, s[12:13]
	s_add_i32 m0, s30, 0x2000
	s_nop 0
	global_load_lds_dwordx4 v[144:145], off
	s_waitcnt vmcnt(6)
	s_barrier
	s_nop 0
	v_mfma_f32_16x16x32_bf16 v[30:33], v[214:217], v[170:173], v[30:33]
	v_mfma_f32_16x16x32_bf16 v[26:29], v[222:225], v[170:173], v[26:29]
	v_mfma_f32_16x16x32_bf16 v[22:25], v[214:217], v[178:181], v[22:25]
	v_mfma_f32_16x16x32_bf16 v[18:21], v[222:225], v[178:181], v[18:21]
	v_mfma_f32_16x16x32_bf16 v[14:17], v[214:217], v[186:189], v[14:17]
	v_mfma_f32_16x16x32_bf16 v[10:13], v[222:225], v[186:189], v[10:13]
	v_mfma_f32_16x16x32_bf16 v[6:9], v[214:217], v[194:197], v[6:9]
	v_mfma_f32_16x16x32_bf16 v[2:5], v[222:225], v[194:197], v[2:5]
	v_mfma_f32_16x16x32_bf16 v[30:33], v[218:221], v[174:177], v[30:33]
	v_mfma_f32_16x16x32_bf16 v[26:29], v[226:229], v[174:177], v[26:29]
	v_mfma_f32_16x16x32_bf16 v[22:25], v[218:221], v[182:185], v[22:25]
	v_mfma_f32_16x16x32_bf16 v[18:21], v[226:229], v[182:185], v[18:21]
	v_mfma_f32_16x16x32_bf16 v[14:17], v[218:221], v[190:193], v[14:17]
	v_mfma_f32_16x16x32_bf16 v[10:13], v[226:229], v[190:193], v[10:13]
	v_mfma_f32_16x16x32_bf16 v[6:9], v[218:221], v[210:213], v[6:9]
	v_mfma_f32_16x16x32_bf16 v[2:5], v[226:229], v[210:213], v[2:5]
	s_nop 0
	s_add_i32 s59, s59, 2
	s_cmp_gt_u32 s59, 29
	s_mov_b64 s[30:31], s[28:29]
	s_barrier
	s_cbranch_scc1 .LBB0_851

; #define PG8_STAGE_B(bufoff, gbase) do { _Pragma("unroll") for (int _i = 0; _i < 2; ++_i) \
;         __builtin_amdgcn_global_load_lds((const unsigned*)((const char*)(gbase) + voffB[_i]), (LAS unsigned*)(lds + (bufoff) + ldsw + _i * 8192), 16, 0, 0); } while (0)
; #define PG8_STAGE_A(bufoff, AO, h, kb) do { _Pragma("unroll") for (int _i = 0; _i < 2; ++_i) \
;         __builtin_amdgcn_global_load_lds((const unsigned*)(S.A + (size_t)(AO)[h][_i] + (size_t)(kb)), (LAS unsigned*)(lds + (bufoff) + ldsw + _i * 8192), 16, 0, 0); } while (0)
; #define PG8_WAIT_V(n) asm volatile("s_waitcnt vmcnt(" #n ")" ::: "memory")
; #define PG8_BAR __builtin_amdgcn_s_barrier()
; #define PG8_AOFF(AO, u, ord) do { _Pragma("unroll") for (int _h = 0; _h < 2; ++_h) _Pragma("unroll") for (int _i = 0; _i < 2; ++_i) \
;         (AO)[_h][_i] = (unsigned)((size_t)S.arow_i((ord), (u), _h * HALF + RA[_i]) * (size_t)K + (size_t)CA[_i]) * 2u; } while (0)
; template <class P>
; __device__ __forceinline__ void gemm_phase(LAS unsigned char* lds, const P& S) {
;     ...
;     Unit cur, nxt; int ui = 0;
;     if (!S.next(0, cur)) return;
;     f32x4 acc[2][2][4][2];
; #pragma unroll
;     for (int a = 0; a < 2; ++a)
; #pragma unroll
;         for (int b = 0; b < 2; ++b)
; #pragma unroll
;             for (int m = 0; m < 4; ++m)
; #pragma unroll
;                 for (int n = 0; n < 2; ++n) acc[a][b][m][n] = (f32x4){0.f, 0.f, 0.f, 0.f};
;     i32x8 At[4], B0[2], B1[2];
;     unsigned ac[2][2], a2[2][2];
;     PG8_AOFF(ac, cur, 0);
;     const char* cB0 = S.bptr(cur, 0); const char* cB1 = S.bptr(cur, 1);
;     PG8_STAGE_B(PG8_SB(0, 0), cB0); PG8_STAGE_A(PG8_SA(0, 0), ac, 0, 0); PG8_STAGE_B(PG8_SB(0, 1), cB1); PG8_STAGE_A(PG8_SA(0, 1), ac, 1, 0);
;     if (wr == 1) PG8_BAR;
;     PG8_WAIT_V(4); PG8_BAR;
;     __device__ __forceinline__ bool next(int i, Unit& u) const {
;         const int NT = ps[32] / 256, NU = NT * 16, L = i * G + c; if (L >= NU) return false;
;         pg8::tile_order(L, NT, 16, u.pm, u.pn); u.e = moe_tile_expert(ps, u.pm); return true;
;     }
;     __device__ __forceinline__ const char* bptr(const Unit& u, int half) const { return (half ? Wu : Wg) + (size_t)u.e * D * D + (size_t)(u.pn * 128) * 16; }
;     __device__ __forceinline__ unsigned arow_i(int ord, const Unit&, int r) const { return (unsigned)gtab[ord * 256 + r]; }
.LBB0_1038:
	s_or_b64 exec, exec, s[2:3]
	s_add_i32 s2, 0, 0x25100
	v_mov_b32_e32 v3, v0
	v_mov_b32_e32 v1, s2
	s_waitcnt lgkmcnt(0)
	s_barrier
	ds_read_b32 v1, v1
	v_readfirstlane_b32 s15, v3
	s_waitcnt lgkmcnt(0)
	v_readfirstlane_b32 s2, v1
	s_ashr_i32 s3, s2, 31
	s_lshr_b32 s3, s3, 24
	s_add_i32 s2, s2, s3
	s_ashr_i32 s5, s2, 8
	s_lshl_b32 s2, s5, 4
	s_cmp_lt_i32 s80, s2
	s_cbranch_scc0 .LBB0_1064
	v_ashrrev_i32_e32 v1, 31, v3
	v_lshrrev_b32_e32 v1, 26, v1
	v_add_u32_e32 v1, v3, v1
	v_ashrrev_i32_e32 v4, 6, v1
	v_bfe_i32 v1, v3, 27, 1
	v_lshlrev_b32_e32 v2, 4, v3
	v_lshrrev_b32_e32 v1, 22, v1
	v_add_u32_e32 v1, v2, v1
	v_and_b32_e32 v1, 0xfffffc00, v1
	v_sub_u32_e32 v1, v2, v1
	v_add_u32_e32 v2, 0x2000, v2
	v_ashrrev_i32_e32 v8, 31, v2
	v_lshrrev_b32_e32 v8, 22, v8
	v_add_u32_e32 v8, v2, v8
	v_ashrrev_i32_e32 v8, 10, v8
	v_mul_i32_i24_e32 v9, 0x400, v8
	v_sub_u32_e32 v2, v2, v9
	v_lshrrev_b32_e32 v9, 4, v2
	v_bitop3_b32 v2, v9, v2, 32 bitop3:0x6c
	v_ashrrev_i32_e32 v10, 31, v2
	v_lshrrev_b32_e32 v10, 26, v10
	v_lshrrev_b32_e32 v5, 4, v1
	v_lshlrev_b32_e32 v9, 3, v8
	v_add_u32_e32 v10, v2, v10
	v_bitop3_b32 v5, v5, v1, 32 bitop3:0x6c
	v_and_b32_e32 v9, -16, v9
	v_ashrrev_i32_e32 v11, 6, v10
	s_ashr_i32 s6, s15, 6
	v_ashrrev_i32_e32 v6, 31, v5
	v_add_u32_e32 v184, v11, v9
	v_and_b32_e32 v9, 0xc0, v10
	s_ashr_i32 s8, s15, 8
	v_lshrrev_b32_e32 v6, 26, v6
	s_lshl_b32 s17, s6, 10
	v_lshlrev_b32_e32 v8, 5, v8
	v_sub_u32_e32 v2, v2, v9
	v_mov_b32_e32 v9, 1
	v_add_u32_e32 v6, v5, v6
	s_add_u32 s33, s86, 0x3000000
	v_and_b32_e32 v8, 32, v8
	v_ashrrev_i16_sdwa v2, v9, sext(v2) dst_sel:DWORD dst_unused:UNUSED_PAD src0_sel:DWORD src1_sel:BYTE_0
	v_lshlrev_b32_e32 v1, 3, v4
	s_addc_u32 s40, s87, 0
	v_add_u32_sdwa v8, v8, sext(v2) dst_sel:DWORD dst_unused:UNUSED_PAD src0_sel:DWORD src1_sel:WORD_0
	v_lshlrev_b32_e32 v2, 5, v4
	v_and_b32_e32 v4, 0xc0, v6
	s_add_u32 s2, s86, 0x69000000
	v_sub_u32_e32 v4, v5, v4
	s_addc_u32 s3, s87, 0
	v_and_b32_e32 v2, 32, v2
	v_ashrrev_i16_sdwa v4, v9, sext(v4) dst_sel:DWORD dst_unused:UNUSED_PAD src0_sel:DWORD src1_sel:BYTE_0
	v_ashrrev_i32_e32 v7, 6, v6
	s_add_u32 s41, s86, 0x13000000
	v_add_u32_sdwa v4, v2, sext(v4) dst_sel:DWORD dst_unused:UNUSED_PAD src0_sel:DWORD src1_sel:WORD_0
	v_and_b32_e32 v2, 3, v11
	s_mov_b32 s14, 0xfffffe0
	v_lshlrev_b32_e32 v5, 1, v184
	v_lshrrev_b32_e32 v6, 2, v184
	s_addc_u32 s42, s87, 0
	s_ashr_i32 s7, s80, 31
	v_and_or_b32 v2, v184, s14, v2
	v_and_b32_e32 v5, 24, v5
	v_and_b32_e32 v6, 4, v6
	v_and_b32_e32 v1, -16, v1
	s_lshr_b32 s7, s7, 29
	v_or3_b32 v2, v2, v5, v6
	v_lshlrev_b32_e32 v5, 8, v8
	v_add_u32_e32 v1, v7, v1
	s_add_i32 s7, s80, s7
	v_and_b32_e32 v5, 0xffff800, v5
	s_ashr_i32 s9, s7, 3
	s_and_b32 s7, s7, -8
	v_add_lshl_u32 v154, v2, v5, 4
	v_and_b32_e32 v2, 3, v7
	v_lshlrev_b32_e32 v5, 1, v1
	v_lshrrev_b32_e32 v6, 2, v1
	s_sub_i32 s7, s80, s7
	v_and_or_b32 v2, v1, s14, v2
	v_and_b32_e32 v5, 24, v5
	v_and_b32_e32 v6, 4, v6
	v_or3_b32 v2, v2, v5, v6
	v_mov_b32_e32 v5, s7
	v_alignbit_b32 v5, s5, v5, 31
	v_lshlrev_b32_e32 v6, 8, v4
	v_readfirstlane_b32 s14, v5
	s_mul_i32 s7, s14, s7
	s_add_i32 s7, s7, s9
	s_ashr_i32 s9, s7, 31
	s_lshr_b32 s9, s9, 25
	s_add_i32 s9, s7, s9
	s_ashr_i32 s14, s9, 7
	s_lshl_b32 s14, s14, 3
	s_sub_i32 s5, s5, s14
	s_min_i32 s5, s5, 8
	s_abs_i32 s16, s5
	v_cvt_f32_u32_e32 v5, s16
	v_and_b32_e32 v6, 0xffff800, v6
	v_add_lshl_u32 v156, v2, v6, 4
	s_sub_i32 s19, 0, s16
	v_rcp_iflag_f32_e32 v2, v5
	s_and_b32 s9, s9, 0xffffff80
	s_sub_i32 s7, s7, s9
	s_abs_i32 s18, s7
	v_mul_f32_e32 v2, 0x4f7ffffe, v2
	v_cvt_u32_f32_e32 v2, v2
	s_xor_b32 s9, s7, s5
	s_ashr_i32 s9, s9, 31
	v_lshlrev_b32_e32 v5, 2, v1
	v_readfirstlane_b32 s20, v2
	s_mul_i32 s19, s19, s20
	s_mul_hi_u32 s19, s20, s19
	s_add_i32 s20, s20, s19
	s_mul_hi_u32 s19, s18, s20
	s_mul_i32 s20, s19, s16
	s_sub_i32 s18, s18, s20
	s_add_i32 s20, s19, 1
	s_sub_i32 s21, s18, s16
	s_cmp_ge_u32 s18, s16
	s_cselect_b32 s19, s20, s19
	s_cselect_b32 s18, s21, s18
	s_add_i32 s20, s19, 1
	s_cmp_ge_u32 s18, s16
	s_cselect_b32 s16, s20, s19
	s_xor_b32 s16, s16, s9
	s_sub_i32 s28, s16, s9
	s_mul_i32 s5, s28, s5
	s_sub_i32 s5, s7, s5
	s_add_i32 s57, s5, s14
	s_lshl_b32 s5, s57, 2
	s_add_i32 s5, s5, 0
	v_lshlrev_b32_e32 v7, 2, v184
	s_add_i32 s5, s5, 0x25140
	v_add_u32_e32 v6, s4, v5
	v_add_u32_e32 v9, s4, v7
	s_add_i32 s4, 0, 0x20200
	v_mov_b32_e32 v2, s5
	v_add_u32_e32 v5, s4, v5
	v_add_u32_e32 v7, s4, v7
	ds_read_b32 v2, v2
	ds_read_b32 v6, v6
	ds_read_b32 v9, v9
	ds_read_b32 v5, v5
	ds_read_b32 v7, v7
	s_waitcnt lgkmcnt(4)
	v_readfirstlane_b32 s4, v2
	s_ashr_i32 s5, s4, 31
	s_lshl_b64 s[4:5], s[4:5], 22
	s_add_u32 s7, s33, s4
	s_addc_u32 s9, s40, s5
	s_lshl_b32 s18, s28, 7
	s_ashr_i32 s19, s18, 31
	s_lshl_b64 s[18:19], s[18:19], 4
	s_add_u32 s30, s7, s18
	s_addc_u32 s31, s9, s19
	s_add_u32 s4, s41, s4
	s_addc_u32 s5, s42, s5
	s_add_i32 s43, s17, 0
	s_add_i32 m0, s43, 0x10000
	v_lshlrev_b32_e32 v185, 1, v4
	global_load_lds_dwordx4 v156, s[30:31]
	s_add_i32 m0, s43, 0x12000
	s_waitcnt lgkmcnt(0)
	v_lshl_add_u32 v166, v6, 11, v185
	v_lshlrev_b32_e32 v186, 1, v8
	global_load_lds_dwordx4 v154, s[30:31]
	s_mov_b32 m0, s43
	s_add_i32 s44, s43, 0x2000
	v_lshl_add_u32 v172, v9, 11, v186
	global_load_lds_dwordx4 v166, s[2:3]
	s_mov_b32 m0, s44
	s_add_u32 s34, s4, s18
	global_load_lds_dwordx4 v172, s[2:3]
	s_addc_u32 s35, s5, s19
	s_add_i32 m0, s43, 0x14000
	s_add_i32 s45, s43, 0x4000
	global_load_lds_dwordx4 v156, s[34:35]
	s_add_i32 m0, s43, 0x16000
	v_lshl_add_u32 v170, v5, 11, v185
	global_load_lds_dwordx4 v154, s[34:35]
	s_mov_b32 m0, s45
	s_add_i32 s46, s43, 0x6000
	v_lshl_add_u32 v168, v7, 11, v186
	global_load_lds_dwordx4 v170, s[2:3]
	s_mov_b32 m0, s46
	v_mov_b32_e32 v159, 0
	global_load_lds_dwordx4 v168, s[2:3]
	v_mov_b32_e32 v167, v159
	v_mov_b32_e32 v173, v159
	v_mov_b32_e32 v157, v159
	v_mov_b32_e32 v155, v159
	v_lshl_add_u64 v[6:7], s[2:3], 0, v[166:167]
	s_cmp_lg_u32 s8, 1
	v_lshl_add_u64 v[4:5], s[2:3], 0, v[172:173]
	s_cbranch_scc1 .LBB0_1041
	s_setprio 1
	s_barrier

; #define PG8_STAGE_B(bufoff, gbase) do { _Pragma("unroll") for (int _i = 0; _i < 2; ++_i) \
;         __builtin_amdgcn_global_load_lds((const unsigned*)((const char*)(gbase) + voffB[_i]), (LAS unsigned*)(lds + (bufoff) + ldsw + _i * 8192), 16, 0, 0); } while (0)
; #define PG8_STAGE_A(bufoff, AO, h, kb) do { _Pragma("unroll") for (int _i = 0; _i < 2; ++_i) \
;         __builtin_amdgcn_global_load_lds((const unsigned*)(S.A + (size_t)(AO)[h][_i] + (size_t)(kb)), (LAS unsigned*)(lds + (bufoff) + ldsw + _i * 8192), 16, 0, 0); } while (0)
; #define PG8_LDA(dst, b, h) do { _Pragma("unroll") for (int m = 0; m < 4; ++m) { dst[m].lo = *(const LAS i32x4*)(lds + PG8_SA(b, h) + aoff + m * 2048); dst[m].hi = *(const LAS i32x4*)(lds + PG8_SA(b, h) + aoff + m * 2048 + 1024); } } while (0)
; #define PG8_LDB(dst, b, h) do { _Pragma("unroll") for (int n = 0; n < 2; ++n) { dst[n].lo = *(const LAS i32x4*)(lds + PG8_SB(b, h) + boff + n * 2048); dst[n].hi = *(const LAS i32x4*)(lds + PG8_SB(b, h) + boff + n * 2048 + 1024); } } while (0)
; #define PG8_BAR __builtin_amdgcn_s_barrier()
; template <class P>
; __device__ __forceinline__ void gemm_phase(LAS unsigned char* lds, const P& S) {
;     ...
;             PG8_LDB(B0, 0, 0); PG8_SCHED; PG8_LDA(At, 0, 0); PG8_STAGE_A(PG8_SA(1, 1), ac, 1, k1);
;             PG8_WAIT_L(8); PG8_BAR; PG8_WAIT_L(0); PG8_MMA(0, 0, At, B0); PG8_BAR; PG8_SCHED;
;             PG8_LDB(B1, 0, 1); PG8_STAGE_B(PG8_SB(0, 0), b20);
;             PG8_BAR; PG8_WAIT_L(0); PG8_MMA(0, 1, At, B1); PG8_BAR;
;             PG8_LDA(At, 0, 1); PG8_STAGE_A(PG8_SA(0, 0), a2, 0, 0);
;             PG8_BAR; PG8_WAIT_L(0); PG8_MMA(1, 0, At, B0); PG8_BAR; PG8_SCHED;
;             PG8_STAGE_B(PG8_SB(0, 1), b21);
;             PG8_WAIT_V(6); PG8_BAR; PG8_MMA(1, 1, At, B1); PG8_BAR;
;             PG8_LDB(B0, 1, 0); PG8_SCHED; PG8_LDA(At, 1, 0); PG8_STAGE_A(PG8_SA(0, 1), a2, 1, 0);
;             PG8_WAIT_L(8); PG8_BAR; PG8_WAIT_L(0); PG8_MMA(0, 0, At, B0); PG8_BAR; PG8_SCHED;
;             PG8_LDB(B1, 1, 1); PG8_STAGE_B(PG8_SB(1, 0), b20 + kstepB);
;             PG8_BAR; PG8_WAIT_L(0); PG8_MMA(0, 1, At, B1); PG8_BAR;
;             PG8_LDA(At, 1, 1); PG8_STAGE_A(PG8_SA(1, 0), a2, 0, kstep);
;             PG8_BAR; PG8_WAIT_L(0); PG8_MMA(1, 0, At, B0); PG8_BAR; PG8_SCHED;
;             PG8_STAGE_B(PG8_SB(1, 1), b21 + kstepB);
;             PG8_WAIT_V(6); PG8_BAR; PG8_MMA(1, 1, At, B1); PG8_BAR;
.LBB0_1046:
	v_add_u32_e32 v14, s13, v173
	ds_read_b128 v[2:5], v14
	ds_read_b128 v[6:9], v14 offset:1024
	ds_read_b128 v[10:13], v14 offset:2048
	ds_read_b128 v[14:17], v14 offset:3072
	s_and_b64 s[34:35], s[34:35], exec
	s_cselect_b32 s39, s21, s61
	s_cselect_b32 s38, s58, s29
	s_cselect_b32 s35, s59, s63
	s_cselect_b32 s34, s60, s62
	v_lshl_add_u64 v[18:19], v[176:177], 0, s[36:37]
	s_add_i32 m0, s43, 0xc000
	ds_read_b128 v[194:197], v189
	ds_read_b128 v[198:201], v189 offset:1024
	ds_read_b128 v[202:205], v189 offset:2048
	ds_read_b128 v[206:209], v189 offset:3072
	ds_read_b128 v[210:213], v189 offset:4096
	ds_read_b128 v[214:217], v189 offset:5120
	ds_read_b128 v[218:221], v189 offset:6144
	ds_read_b128 v[222:225], v189 offset:7168
	global_load_lds_dwordx4 v[18:19], off
	v_lshl_add_u64 v[18:19], v[178:179], 0, s[36:37]
	s_add_i32 m0, s43, 0xe000
	s_nop 0
	global_load_lds_dwordx4 v[18:19], off
	s_waitcnt lgkmcnt(8)
	s_barrier
	s_waitcnt lgkmcnt(0)
	s_nop 0
	s_waitcnt lgkmcnt(0)
	v_mfma_f32_16x16x128_f8f6f4 v[150:153], v[2:9], v[194:201], v[150:153]
	v_mfma_f32_16x16x128_f8f6f4 v[142:145], v[10:17], v[194:201], v[142:145]
	v_mfma_f32_16x16x128_f8f6f4 v[134:137], v[2:9], v[202:209], v[134:137]
	v_mfma_f32_16x16x128_f8f6f4 v[126:129], v[10:17], v[202:209], v[126:129]
	v_mfma_f32_16x16x128_f8f6f4 v[118:121], v[2:9], v[210:217], v[118:121]
	v_mfma_f32_16x16x128_f8f6f4 v[110:113], v[10:17], v[210:217], v[110:113]
	v_mfma_f32_16x16x128_f8f6f4 v[102:105], v[2:9], v[218:225], v[102:105]
	v_mfma_f32_16x16x128_f8f6f4 v[94:97], v[10:17], v[218:225], v[94:97]
	s_nop 0
	s_barrier
	s_add_i32 s36, s13, s17
	v_add_u32_e32 v165, s50, v173
	v_lshl_add_u64 v[180:181], s[38:39], 0, v[156:157]
	s_mov_b32 m0, s36
	ds_read_b128 v[18:21], v165
	ds_read_b128 v[22:25], v165 offset:1024
	ds_read_b128 v[226:229], v165 offset:2048
	ds_read_b128 v[230:233], v165 offset:3072
	global_load_lds_dwordx4 v[180:181], off
	v_lshl_add_u64 v[180:181], s[38:39], 0, v[154:155]
	s_add_i32 m0, s36, 0x2000
	s_nop 0
	global_load_lds_dwordx4 v[180:181], off
	s_barrier
	s_waitcnt lgkmcnt(0)
	s_nop 0
	s_waitcnt lgkmcnt(0)
	v_mfma_f32_16x16x128_f8f6f4 v[146:149], v[18:25], v[194:201], v[146:149]
	v_mfma_f32_16x16x128_f8f6f4 v[138:141], v[226:233], v[194:201], v[138:141]
	v_mfma_f32_16x16x128_f8f6f4 v[130:133], v[18:25], v[202:209], v[130:133]
	v_mfma_f32_16x16x128_f8f6f4 v[122:125], v[226:233], v[202:209], v[122:125]
	v_mfma_f32_16x16x128_f8f6f4 v[114:117], v[18:25], v[210:217], v[114:117]
	v_mfma_f32_16x16x128_f8f6f4 v[106:109], v[226:233], v[210:217], v[106:109]
	v_mfma_f32_16x16x128_f8f6f4 v[98:101], v[18:25], v[218:225], v[98:101]
	v_mfma_f32_16x16x128_f8f6f4 v[90:93], v[226:233], v[218:225], v[90:93]
	s_nop 0
	s_mov_b32 m0, s43
	s_barrier
	ds_read_b128 v[194:197], v189 offset:16384
	ds_read_b128 v[198:201], v189 offset:17408
	ds_read_b128 v[202:205], v189 offset:18432
	ds_read_b128 v[206:209], v189 offset:19456
	ds_read_b128 v[210:213], v189 offset:20480
	ds_read_b128 v[214:217], v189 offset:21504
	ds_read_b128 v[218:221], v189 offset:22528
	ds_read_b128 v[222:225], v189 offset:23552
	global_load_lds_dwordx4 v158, s[2:3]
	s_mov_b32 m0, s44
	v_mov_b32_e32 v165, v159
	global_load_lds_dwordx4 v164, s[2:3]
	s_barrier
	s_waitcnt lgkmcnt(0)
	v_lshl_add_u64 v[182:183], s[2:3], 0, v[158:159]
	v_lshl_add_u64 v[180:181], s[2:3], 0, v[164:165]
	s_nop 0
	s_waitcnt lgkmcnt(0)
	v_mfma_f32_16x16x128_f8f6f4 v[86:89], v[2:9], v[194:201], v[86:89]
	v_mfma_f32_16x16x128_f8f6f4 v[78:81], v[10:17], v[194:201], v[78:81]
	v_mfma_f32_16x16x128_f8f6f4 v[70:73], v[2:9], v[202:209], v[70:73]
	v_mfma_f32_16x16x128_f8f6f4 v[62:65], v[10:17], v[202:209], v[62:65]
	v_mfma_f32_16x16x128_f8f6f4 v[54:57], v[2:9], v[210:217], v[54:57]
	v_mfma_f32_16x16x128_f8f6f4 v[46:49], v[10:17], v[210:217], v[46:49]
	v_mfma_f32_16x16x128_f8f6f4 v[38:41], v[2:9], v[218:225], v[38:41]
	v_mfma_f32_16x16x128_f8f6f4 v[34:37], v[10:17], v[218:225], v[34:37]
	s_nop 0
	s_barrier
	s_add_i32 s36, s50, s17
	v_lshl_add_u64 v[2:3], s[34:35], 0, v[156:157]
	s_mov_b32 m0, s36
	s_nop 0
	global_load_lds_dwordx4 v[2:3], off
	v_lshl_add_u64 v[2:3], s[34:35], 0, v[154:155]
	s_add_i32 m0, s36, 0x2000
	s_nop 0
	global_load_lds_dwordx4 v[2:3], off
	s_waitcnt vmcnt(6)
	s_barrier
	s_nop 0
	v_mfma_f32_16x16x128_f8f6f4 v[82:85], v[18:25], v[194:201], v[82:85]
	v_mfma_f32_16x16x128_f8f6f4 v[74:77], v[226:233], v[194:201], v[74:77]
	v_mfma_f32_16x16x128_f8f6f4 v[66:69], v[18:25], v[202:209], v[66:69]
	v_mfma_f32_16x16x128_f8f6f4 v[58:61], v[226:233], v[202:209], v[58:61]
	v_mfma_f32_16x16x128_f8f6f4 v[50:53], v[18:25], v[210:217], v[50:53]
	v_mfma_f32_16x16x128_f8f6f4 v[42:45], v[226:233], v[210:217], v[42:45]
	v_mfma_f32_16x16x128_f8f6f4 v[30:33], v[18:25], v[218:225], v[30:33]
	v_mfma_f32_16x16x128_f8f6f4 v[26:29], v[226:233], v[218:225], v[26:29]
	s_nop 0
	s_add_i32 s65, 0, 0x18000
	v_add_u32_e32 v14, s65, v173
	s_barrier
; #define PG8_STAGE_B(bufoff, gbase) do { _Pragma("unroll") for (int _i = 0; _i < 2; ++_i) \
;         __builtin_amdgcn_global_load_lds((const unsigned*)((const char*)(gbase) + voffB[_i]), (LAS unsigned*)(lds + (bufoff) + ldsw + _i * 8192), 16, 0, 0); } while (0)
; #define PG8_STAGE_A(bufoff, AO, h, kb) do { _Pragma("unroll") for (int _i = 0; _i < 2; ++_i) \
;         __builtin_amdgcn_global_load_lds((const unsigned*)(S.A + (size_t)(AO)[h][_i] + (size_t)(kb)), (LAS unsigned*)(lds + (bufoff) + ldsw + _i * 8192), 16, 0, 0); } while (0)
; #define PG8_LDA(dst, b, h) do { _Pragma("unroll") for (int m = 0; m < 4; ++m) { dst[m].lo = *(const LAS i32x4*)(lds + PG8_SA(b, h) + aoff + m * 2048); dst[m].hi = *(const LAS i32x4*)(lds + PG8_SA(b, h) + aoff + m * 2048 + 1024); } } while (0)
; #define PG8_LDB(dst, b, h) do { _Pragma("unroll") for (int n = 0; n < 2; ++n) { dst[n].lo = *(const LAS i32x4*)(lds + PG8_SB(b, h) + boff + n * 2048); dst[n].hi = *(const LAS i32x4*)(lds + PG8_SB(b, h) + boff + n * 2048 + 1024); } } while (0)
; #define PG8_BAR __builtin_amdgcn_s_barrier()
; template <class P>
; __device__ __forceinline__ void gemm_phase(LAS unsigned char* lds, const P& S) {
;     ...
;             PG8_LDB(B0, 0, 0); PG8_SCHED; PG8_LDA(At, 0, 0); PG8_STAGE_A(PG8_SA(1, 1), ac, 1, k1);
;             PG8_WAIT_L(8); PG8_BAR; PG8_WAIT_L(0); PG8_MMA(0, 0, At, B0); PG8_BAR; PG8_SCHED;
;             PG8_LDB(B1, 0, 1); PG8_STAGE_B(PG8_SB(0, 0), b20);
;             PG8_BAR; PG8_WAIT_L(0); PG8_MMA(0, 1, At, B1); PG8_BAR;
;             PG8_LDA(At, 0, 1); PG8_STAGE_A(PG8_SA(0, 0), a2, 0, 0);
;             PG8_BAR; PG8_WAIT_L(0); PG8_MMA(1, 0, At, B0); PG8_BAR; PG8_SCHED;
;             PG8_STAGE_B(PG8_SB(0, 1), b21);
;             PG8_WAIT_V(6); PG8_BAR; PG8_MMA(1, 1, At, B1); PG8_BAR;
;             PG8_LDB(B0, 1, 0); PG8_SCHED; PG8_LDA(At, 1, 0); PG8_STAGE_A(PG8_SA(0, 1), a2, 1, 0);
;             PG8_WAIT_L(8); PG8_BAR; PG8_WAIT_L(0); PG8_MMA(0, 0, At, B0); PG8_BAR; PG8_SCHED;
;             PG8_LDB(B1, 1, 1); PG8_STAGE_B(PG8_SB(1, 0), b20 + kstepB);
;             PG8_BAR; PG8_WAIT_L(0); PG8_MMA(0, 1, At, B1); PG8_BAR;
;             PG8_LDA(At, 1, 1); PG8_STAGE_A(PG8_SA(1, 0), a2, 0, kstep);
;             PG8_BAR; PG8_WAIT_L(0); PG8_MMA(1, 0, At, B0); PG8_BAR; PG8_SCHED;
;             PG8_STAGE_B(PG8_SB(1, 1), b21 + kstepB);
;             PG8_WAIT_V(6); PG8_BAR; PG8_MMA(1, 1, At, B1); PG8_BAR;
	ds_read_b128 v[2:5], v14
	ds_read_b128 v[6:9], v14 offset:1024
	ds_read_b128 v[10:13], v14 offset:2048
	ds_read_b128 v[14:17], v14 offset:3072
	s_mov_b32 m0, s45
	ds_read_b128 v[18:21], v189 offset:32768
	ds_read_b128 v[22:25], v189 offset:33792
	ds_read_b128 v[194:197], v189 offset:34816
	ds_read_b128 v[198:201], v189 offset:35840
	ds_read_b128 v[202:205], v189 offset:36864
	ds_read_b128 v[206:209], v189 offset:37888
	ds_read_b128 v[210:213], v189 offset:38912
	ds_read_b128 v[214:217], v189 offset:39936
	global_load_lds_dwordx4 v169, s[2:3]
	s_mov_b32 m0, s46
	s_nop 0
	global_load_lds_dwordx4 v171, s[2:3]
	s_waitcnt lgkmcnt(8)
	s_barrier
	s_waitcnt lgkmcnt(0)
	s_nop 0
	s_waitcnt lgkmcnt(0)
	v_mfma_f32_16x16x128_f8f6f4 v[150:153], v[2:9], v[18:25], v[150:153]
	v_mfma_f32_16x16x128_f8f6f4 v[142:145], v[10:17], v[18:25], v[142:145]
	v_mfma_f32_16x16x128_f8f6f4 v[134:137], v[2:9], v[194:201], v[134:137]
	v_mfma_f32_16x16x128_f8f6f4 v[126:129], v[10:17], v[194:201], v[126:129]
	v_mfma_f32_16x16x128_f8f6f4 v[118:121], v[2:9], v[202:209], v[118:121]
	v_mfma_f32_16x16x128_f8f6f4 v[110:113], v[10:17], v[202:209], v[110:113]
	v_mfma_f32_16x16x128_f8f6f4 v[102:105], v[2:9], v[210:217], v[102:105]
	v_mfma_f32_16x16x128_f8f6f4 v[94:97], v[10:17], v[210:217], v[94:97]
	s_nop 0
	s_barrier
	s_add_i32 s66, 0, 0x1c000
	s_add_u32 s36, s38, 0x40000
	s_addc_u32 s37, s39, 0
	s_add_i32 s38, s65, s17
	v_add_u32_e32 v165, s66, v173
	v_lshl_add_u64 v[234:235], s[36:37], 0, v[156:157]
	s_mov_b32 m0, s38
	ds_read_b128 v[218:221], v165
	ds_read_b128 v[222:225], v165 offset:1024
	ds_read_b128 v[226:229], v165 offset:2048
	ds_read_b128 v[230:233], v165 offset:3072
	global_load_lds_dwordx4 v[234:235], off
	v_lshl_add_u64 v[234:235], s[36:37], 0, v[154:155]
	s_add_i32 m0, s38, 0x2000
	s_nop 0
	global_load_lds_dwordx4 v[234:235], off
	s_barrier
	s_waitcnt lgkmcnt(0)
	s_nop 0
	s_waitcnt lgkmcnt(0)
	v_mfma_f32_16x16x128_f8f6f4 v[146:149], v[218:225], v[18:25], v[146:149]
	v_mfma_f32_16x16x128_f8f6f4 v[138:141], v[226:233], v[18:25], v[138:141]
	v_mfma_f32_16x16x128_f8f6f4 v[130:133], v[218:225], v[194:201], v[130:133]
	v_mfma_f32_16x16x128_f8f6f4 v[122:125], v[226:233], v[194:201], v[122:125]
	v_mfma_f32_16x16x128_f8f6f4 v[114:117], v[218:225], v[202:209], v[114:117]
	v_mfma_f32_16x16x128_f8f6f4 v[106:109], v[226:233], v[202:209], v[106:109]
	v_mfma_f32_16x16x128_f8f6f4 v[98:101], v[218:225], v[210:217], v[98:101]
	v_mfma_f32_16x16x128_f8f6f4 v[90:93], v[226:233], v[210:217], v[90:93]
	s_nop 0
	s_mov_b32 m0, s47
	v_lshl_add_u64 v[182:183], v[182:183], 0, s[6:7]
	s_barrier
	ds_read_b128 v[18:21], v189 offset:49152
	ds_read_b128 v[22:25], v189 offset:50176
	ds_read_b128 v[194:197], v189 offset:51200
	ds_read_b128 v[198:201], v189 offset:52224
	ds_read_b128 v[202:205], v189 offset:53248
	ds_read_b128 v[206:209], v189 offset:54272
	ds_read_b128 v[210:213], v189 offset:55296
	ds_read_b128 v[214:217], v189 offset:56320
	global_load_lds_dwordx4 v[182:183], off
	v_lshl_add_u64 v[180:181], v[180:181], 0, s[6:7]
	s_mov_b32 m0, s48
	s_nop 0
	global_load_lds_dwordx4 v[180:181], off
	s_barrier
	s_waitcnt lgkmcnt(0)
	s_nop 0
	s_waitcnt lgkmcnt(0)
	v_mfma_f32_16x16x128_f8f6f4 v[86:89], v[2:9], v[18:25], v[86:89]
	v_mfma_f32_16x16x128_f8f6f4 v[78:81], v[10:17], v[18:25], v[78:81]
	v_mfma_f32_16x16x128_f8f6f4 v[70:73], v[2:9], v[194:201], v[70:73]
	v_mfma_f32_16x16x128_f8f6f4 v[62:65], v[10:17], v[194:201], v[62:65]
	v_mfma_f32_16x16x128_f8f6f4 v[54:57], v[2:9], v[202:209], v[54:57]
	v_mfma_f32_16x16x128_f8f6f4 v[46:49], v[10:17], v[202:209], v[46:49]
	v_mfma_f32_16x16x128_f8f6f4 v[38:41], v[2:9], v[210:217], v[38:41]
	v_mfma_f32_16x16x128_f8f6f4 v[34:37], v[10:17], v[210:217], v[34:37]
	s_nop 0
	s_barrier
	s_add_u32 s34, s34, 0x40000
	s_addc_u32 s35, s35, 0
	s_add_i32 s36, s66, s17
	v_lshl_add_u64 v[2:3], s[34:35], 0, v[156:157]
	s_mov_b32 m0, s36
	s_nop 0
	global_load_lds_dwordx4 v[2:3], off
	v_lshl_add_u64 v[2:3], s[34:35], 0, v[154:155]
	s_add_i32 m0, s36, 0x2000
	s_nop 0
	global_load_lds_dwordx4 v[2:3], off
	s_waitcnt vmcnt(6)
	s_barrier
	s_nop 0
	v_mfma_f32_16x16x128_f8f6f4 v[82:85], v[218:225], v[18:25], v[82:85]
	v_mfma_f32_16x16x128_f8f6f4 v[74:77], v[226:233], v[18:25], v[74:77]
	v_mfma_f32_16x16x128_f8f6f4 v[66:69], v[218:225], v[194:201], v[66:69]
	v_mfma_f32_16x16x128_f8f6f4 v[58:61], v[226:233], v[194:201], v[58:61]
	v_mfma_f32_16x16x128_f8f6f4 v[50:53], v[218:225], v[202:209], v[50:53]
	v_mfma_f32_16x16x128_f8f6f4 v[42:45], v[226:233], v[202:209], v[42:45]
	v_mfma_f32_16x16x128_f8f6f4 v[30:33], v[218:225], v[210:217], v[30:33]
	v_mfma_f32_16x16x128_f8f6f4 v[26:29], v[226:233], v[210:217], v[26:29]
	s_nop 0
	s_add_i32 s64, s64, 2
	s_add_u32 s29, s29, 0x80000
	s_addc_u32 s61, s61, 0
	s_add_u32 s62, s62, 0x80000
	s_addc_u32 s63, s63, 0
	s_cmp_gt_u32 s64, 13
	s_mov_b64 s[36:37], s[30:31]
	s_barrier
	s_cbranch_scc1 .LBB0_1042

; #define PG8_STAGE_B(bufoff, gbase) do { _Pragma("unroll") for (int _i = 0; _i < 2; ++_i) \
;         __builtin_amdgcn_global_load_lds((const unsigned*)((const char*)(gbase) + voffB[_i]), (LAS unsigned*)(lds + (bufoff) + ldsw + _i * 8192), 16, 0, 0); } while (0)
; #define PG8_STAGE_A(bufoff, AO, h, kb) do { _Pragma("unroll") for (int _i = 0; _i < 2; ++_i) \
;         __builtin_amdgcn_global_load_lds((const unsigned*)(S.A + (size_t)(AO)[h][_i] + (size_t)(kb)), (LAS unsigned*)(lds + (bufoff) + ldsw + _i * 8192), 16, 0, 0); } while (0)
; #define PG8_WAIT_V(n) asm volatile("s_waitcnt vmcnt(" #n ")" ::: "memory")
; #define PG8_BAR __builtin_amdgcn_s_barrier()
; #define PG8_AOFF(AO, u, ord) do { _Pragma("unroll") for (int _h = 0; _h < 2; ++_h) _Pragma("unroll") for (int _i = 0; _i < 2; ++_i) \
;         (AO)[_h][_i] = (unsigned)((size_t)S.arow_i((ord), (u), _h * HALF + RA[_i]) * (size_t)K + (size_t)CA[_i]) * 2u; } while (0)
;     __device__ __forceinline__ unsigned arow_i(int, const Unit& u, int r) const { return (unsigned)(u.pm * 256 + r); }
; template <class P>
; __device__ __forceinline__ void gemm_phase(LAS unsigned char* lds, const P& S) {
;     ...
;     Unit cur, nxt; int ui = 0;
;     if (!S.next(0, cur)) return;
;     f32x4 acc[2][2][4][2];
; #pragma unroll
;     for (int a = 0; a < 2; ++a)
; #pragma unroll
;         for (int b = 0; b < 2; ++b)
; #pragma unroll
;             for (int m = 0; m < 4; ++m)
; #pragma unroll
;                 for (int n = 0; n < 2; ++n) acc[a][b][m][n] = (f32x4){0.f, 0.f, 0.f, 0.f};
;     i32x8 At[4], B0[2], B1[2];
;     unsigned ac[2][2], a2[2][2];
;     PG8_AOFF(ac, cur, 0);
;     const char* cB0 = S.bptr(cur, 0); const char* cB1 = S.bptr(cur, 1);
;     PG8_STAGE_B(PG8_SB(0, 0), cB0); PG8_STAGE_A(PG8_SA(0, 0), ac, 0, 0); PG8_STAGE_B(PG8_SB(0, 1), cB1); PG8_STAGE_A(PG8_SA(0, 1), ac, 1, 0);
;     if (wr == 1) PG8_BAR;
;     PG8_WAIT_V(4); PG8_BAR;
;     __device__ __forceinline__ bool next(int i, Unit& u) const {
;         const int NT = ps[32] / 256, NU = NT * 8, L = i * G + c; if (L >= NU) return false;
;         pg8::tile_order(L, NT, 8, u.pm, u.pn); u.e = moe_tile_expert(ps, u.pm); return true;
;     }
;     __device__ __forceinline__ unsigned arow_i(int, const Unit& u, int r) const { return (unsigned)(u.pm * 256 + r); }
.LBB0_1114:
	s_cmp_lt_i32 s68, 11
	s_cselect_b64 s[0:1], -1, 0
	s_and_b64 s[2:3], s[0:1], s[2:3]
	s_andn2_b64 vcc, exec, s[2:3]
	s_cbranch_vccnz .LBB0_1133
	s_add_i32 s2, 0, 0x25100
	s_waitcnt vmcnt(0)
	v_mov_b32_e32 v3, v0
	v_mov_b32_e32 v1, s2
	ds_read_b32 v1, v1
	v_readfirstlane_b32 s17, v3
	s_waitcnt lgkmcnt(0)
	v_readfirstlane_b32 s2, v1
	s_ashr_i32 s3, s2, 31
	s_lshr_b32 s3, s3, 24
	s_add_i32 s2, s2, s3
	s_ashr_i32 s4, s2, 8
	s_lshl_b32 s2, s4, 3
	s_cmp_ge_i32 s80, s2
	s_cbranch_scc1 .LBB0_1133
	v_ashrrev_i32_e32 v1, 31, v3
	v_lshrrev_b32_e32 v1, 26, v1
	v_add_u32_e32 v1, v3, v1
	v_ashrrev_i32_e32 v4, 6, v1
	v_bfe_i32 v1, v3, 27, 1
	v_lshlrev_b32_e32 v2, 4, v3
	v_lshrrev_b32_e32 v1, 22, v1
	v_add_u32_e32 v1, v2, v1
	v_and_b32_e32 v1, 0xfffffc00, v1
	v_sub_u32_e32 v1, v2, v1
	v_add_u32_e32 v2, 0x2000, v2
	v_ashrrev_i32_e32 v8, 31, v2
	v_lshrrev_b32_e32 v8, 22, v8
	v_add_u32_e32 v8, v2, v8
	v_ashrrev_i32_e32 v8, 10, v8
	s_add_u32 s2, s86, 0x37200000
	v_mul_i32_i24_e32 v9, 0x400, v8
	s_addc_u32 s3, s87, 0
	v_sub_u32_e32 v2, v2, v9
	s_add_u32 s19, s86, 0x23000000
	v_lshrrev_b32_e32 v9, 4, v2
	s_addc_u32 s33, s87, 0
	v_bitop3_b32 v2, v9, v2, 32 bitop3:0x6c
	s_ashr_i32 s5, s80, 31
	v_ashrrev_i32_e32 v10, 31, v2
	s_lshr_b32 s5, s5, 29
	v_lshrrev_b32_e32 v10, 26, v10
	s_add_i32 s5, s80, s5
	v_lshrrev_b32_e32 v5, 4, v1
	v_lshlrev_b32_e32 v9, 3, v8
	v_add_u32_e32 v10, v2, v10
	s_ashr_i32 s7, s5, 3
	s_and_b32 s5, s5, -8
	v_bitop3_b32 v5, v5, v1, 32 bitop3:0x6c
	v_and_b32_e32 v9, -16, v9
	v_ashrrev_i32_e32 v11, 6, v10
	s_sub_i32 s5, s80, s5
	v_ashrrev_i32_e32 v6, 31, v5
	v_add_u32_e32 v182, v11, v9
	v_and_b32_e32 v9, 0xc0, v10
	s_lshr_b32 s8, s5, 31
	v_lshrrev_b32_e32 v6, 26, v6
	v_lshlrev_b32_e32 v8, 5, v8
	v_sub_u32_e32 v2, v2, v9
	v_mov_b32_e32 v9, 1
	s_add_i32 s8, s4, s8
	v_add_u32_e32 v6, v5, v6
	v_and_b32_e32 v8, 32, v8
	v_ashrrev_i16_sdwa v2, v9, sext(v2) dst_sel:DWORD dst_unused:UNUSED_PAD src0_sel:DWORD src1_sel:BYTE_0
	s_mul_i32 s5, s8, s5
	v_lshlrev_b32_e32 v1, 3, v4
	v_add_u32_sdwa v8, v8, sext(v2) dst_sel:DWORD dst_unused:UNUSED_PAD src0_sel:DWORD src1_sel:WORD_0
	v_lshlrev_b32_e32 v2, 5, v4
	v_and_b32_e32 v4, 0xc0, v6
	s_add_i32 s5, s5, s7
	v_sub_u32_e32 v4, v5, v4
	s_ashr_i32 s7, s5, 31
	v_and_b32_e32 v2, 32, v2
	v_ashrrev_i16_sdwa v4, v9, sext(v4) dst_sel:DWORD dst_unused:UNUSED_PAD src0_sel:DWORD src1_sel:BYTE_0
	s_lshr_b32 s7, s7, 26
	v_ashrrev_i32_e32 v7, 6, v6
	v_add_u32_sdwa v4, v2, sext(v4) dst_sel:DWORD dst_unused:UNUSED_PAD src0_sel:DWORD src1_sel:WORD_0
	v_and_b32_e32 v2, 3, v11
	s_mov_b32 s9, 0xfffffe0
	v_lshlrev_b32_e32 v5, 1, v182
	v_lshrrev_b32_e32 v6, 2, v182
	s_add_i32 s7, s5, s7
	v_and_or_b32 v2, v182, s9, v2
	v_and_b32_e32 v5, 24, v5
	v_and_b32_e32 v6, 4, v6
	s_ashr_i32 s8, s7, 6
	v_or3_b32 v2, v2, v5, v6
	v_lshlrev_b32_e32 v5, 8, v8
	s_lshl_b32 s8, s8, 3
	v_and_b32_e32 v1, -16, v1
	v_and_b32_e32 v5, 0xffff800, v5
	s_sub_i32 s4, s4, s8
	v_add_u32_e32 v1, v7, v1
	v_add_lshl_u32 v154, v2, v5, 4
	v_and_b32_e32 v2, 3, v7
	s_min_i32 s4, s4, 8
	v_and_or_b32 v5, v1, s9, v2
	s_abs_i32 s9, s4
	v_cvt_f32_u32_e32 v6, s9
	v_lshlrev_b32_e32 v2, 1, v1
	v_and_b32_e32 v7, 24, v2
	v_lshrrev_b32_e32 v2, 2, v1
	v_and_b32_e32 v9, 4, v2
	v_rcp_iflag_f32_e32 v2, v6
	s_sub_i32 s12, 0, s9
	s_andn2_b32 s7, s7, 63
	s_sub_i32 s5, s5, s7
	v_mul_f32_e32 v2, 0x4f7ffffe, v2
	v_cvt_u32_f32_e32 v2, v2
	s_abs_i32 s11, s5
	s_ashr_i32 s6, s17, 6
	s_xor_b32 s7, s5, s4
	v_readfirstlane_b32 s13, v2
	s_mul_i32 s12, s12, s13
	s_mul_hi_u32 s12, s13, s12
	s_add_i32 s13, s13, s12
	s_mul_hi_u32 s12, s11, s13
	s_mul_i32 s13, s12, s9
	s_sub_i32 s11, s11, s13
	s_ashr_i32 s10, s17, 8
	s_lshl_b32 s48, s6, 10
	s_ashr_i32 s7, s7, 31
	s_add_i32 s13, s12, 1
	s_sub_i32 s14, s11, s9
	s_cmp_ge_u32 s11, s9
	s_cselect_b32 s12, s13, s12
	s_cselect_b32 s11, s14, s11
	s_add_i32 s13, s12, 1
	s_cmp_ge_u32 s11, s9
	s_cselect_b32 s9, s13, s12
	s_xor_b32 s9, s9, s7
	s_sub_i32 s38, s9, s7
	s_mul_i32 s4, s38, s4
	s_sub_i32 s4, s5, s4
	s_add_i32 s65, s4, s8
	s_lshl_b32 s4, s65, 2
	s_add_i32 s4, s4, 0
	s_add_i32 s4, s4, 0x25140
	v_mov_b32_e32 v2, s4
	ds_read_b32 v2, v2
	v_lshlrev_b32_e32 v6, 8, v4
	v_or3_b32 v5, v5, v7, v9
	v_and_b32_e32 v6, 0xffff800, v6
	s_lshl_b32 s7, s65, 8
	s_waitcnt lgkmcnt(0)
	v_readfirstlane_b32 s4, v2
	v_add_lshl_u32 v156, v5, v6, 4
	s_ashr_i32 s5, s4, 31
	v_add_u32_e32 v5, s7, v1
	v_lshlrev_b32_e32 v183, 1, v4
	v_add_u32_e32 v4, s7, v182
	v_lshlrev_b32_e32 v184, 1, v8
	s_bitset1_b32 s7, 7
	v_lshl_add_u32 v164, v4, 11, v184
	v_add_u32_e32 v4, s7, v1
	s_lshl_b64 s[4:5], s[4:5], 22
	v_lshl_add_u32 v166, v4, 11, v183
	v_add_u32_e32 v4, s7, v182
	s_add_u32 s7, s19, s4
	s_addc_u32 s11, s33, s5
	s_lshl_b32 s4, s38, 8
	s_ashr_i32 s5, s4, 31
	s_lshl_b64 s[8:9], s[4:5], 4
	s_add_u32 s40, s7, s8
	s_addc_u32 s41, s11, s9
	s_add_i32 s49, s48, 0
	s_bitset1_b32 s4, 7
	s_add_i32 m0, s49, 0x10000
	s_ashr_i32 s5, s4, 31
	global_load_lds_dwordx4 v156, s[40:41]
	s_add_i32 m0, s49, 0x12000
	v_lshl_add_u32 v162, v5, 11, v183
	s_lshl_b64 s[4:5], s[4:5], 4
	global_load_lds_dwordx4 v154, s[40:41]
	s_mov_b32 m0, s49
	s_add_i32 s50, s49, 0x2000
	global_load_lds_dwordx4 v162, s[2:3]
	s_mov_b32 m0, s50
	s_add_u32 s42, s7, s4
	global_load_lds_dwordx4 v164, s[2:3]
	s_addc_u32 s43, s11, s5
	s_add_i32 m0, s49, 0x14000
	s_add_i32 s51, s49, 0x4000
	global_load_lds_dwordx4 v156, s[42:43]
	s_add_i32 m0, s49, 0x16000
	s_add_i32 s52, s49, 0x6000
	global_load_lds_dwordx4 v154, s[42:43]
	s_mov_b32 m0, s51
	v_lshl_add_u32 v168, v4, 11, v184
	global_load_lds_dwordx4 v166, s[2:3]
	s_mov_b32 m0, s52
	v_mov_b32_e32 v159, 0
	global_load_lds_dwordx4 v168, s[2:3]
	v_mov_b32_e32 v163, v159
	v_mov_b32_e32 v165, v159
	v_mov_b32_e32 v157, v159
	v_mov_b32_e32 v155, v159
	v_lshl_add_u64 v[6:7], s[2:3], 0, v[162:163]
	s_cmp_lg_u32 s10, 1
	v_lshl_add_u64 v[4:5], s[2:3], 0, v[164:165]
	s_cbranch_scc1 .LBB0_1118
	s_setprio 1
	s_barrier

; #define PG8_STAGE_B(bufoff, gbase) do { _Pragma("unroll") for (int _i = 0; _i < 2; ++_i) \
;         __builtin_amdgcn_global_load_lds((const unsigned*)((const char*)(gbase) + voffB[_i]), (LAS unsigned*)(lds + (bufoff) + ldsw + _i * 8192), 16, 0, 0); } while (0)
; #define PG8_STAGE_A(bufoff, AO, h, kb) do { _Pragma("unroll") for (int _i = 0; _i < 2; ++_i) \
;         __builtin_amdgcn_global_load_lds((const unsigned*)(S.A + (size_t)(AO)[h][_i] + (size_t)(kb)), (LAS unsigned*)(lds + (bufoff) + ldsw + _i * 8192), 16, 0, 0); } while (0)
; #define PG8_LDA(dst, b, h) do { _Pragma("unroll") for (int m = 0; m < 4; ++m) { dst[m].lo = *(const LAS i32x4*)(lds + PG8_SA(b, h) + aoff + m * 2048); dst[m].hi = *(const LAS i32x4*)(lds + PG8_SA(b, h) + aoff + m * 2048 + 1024); } } while (0)
; #define PG8_LDB(dst, b, h) do { _Pragma("unroll") for (int n = 0; n < 2; ++n) { dst[n].lo = *(const LAS i32x4*)(lds + PG8_SB(b, h) + boff + n * 2048); dst[n].hi = *(const LAS i32x4*)(lds + PG8_SB(b, h) + boff + n * 2048 + 1024); } } while (0)
; #define PG8_BAR __builtin_amdgcn_s_barrier()
; template <class P>
; __device__ __forceinline__ void gemm_phase(LAS unsigned char* lds, const P& S) {
;     ...
;             PG8_LDB(B0, 0, 0); PG8_SCHED; PG8_LDA(At, 0, 0); PG8_STAGE_A(PG8_SA(1, 1), ac, 1, k1);
;             PG8_WAIT_L(8); PG8_BAR; PG8_WAIT_L(0); PG8_MMA(0, 0, At, B0); PG8_BAR; PG8_SCHED;
;             PG8_LDB(B1, 0, 1); PG8_STAGE_B(PG8_SB(0, 0), b20);
;             PG8_BAR; PG8_WAIT_L(0); PG8_MMA(0, 1, At, B1); PG8_BAR;
;             PG8_LDA(At, 0, 1); PG8_STAGE_A(PG8_SA(0, 0), a2, 0, 0);
;             PG8_BAR; PG8_WAIT_L(0); PG8_MMA(1, 0, At, B0); PG8_BAR; PG8_SCHED;
;             PG8_STAGE_B(PG8_SB(0, 1), b21);
;             PG8_WAIT_V(6); PG8_BAR; PG8_MMA(1, 1, At, B1); PG8_BAR;
;             PG8_LDB(B0, 1, 0); PG8_SCHED; PG8_LDA(At, 1, 0); PG8_STAGE_A(PG8_SA(0, 1), a2, 1, 0);
;             PG8_WAIT_L(8); PG8_BAR; PG8_WAIT_L(0); PG8_MMA(0, 0, At, B0); PG8_BAR; PG8_SCHED;
;             PG8_LDB(B1, 1, 1); PG8_STAGE_B(PG8_SB(1, 0), b20 + kstepB);
;             PG8_BAR; PG8_WAIT_L(0); PG8_MMA(0, 1, At, B1); PG8_BAR;
;             PG8_LDA(At, 1, 1); PG8_STAGE_A(PG8_SA(1, 0), a2, 0, kstep);
;             PG8_BAR; PG8_WAIT_L(0); PG8_MMA(1, 0, At, B0); PG8_BAR; PG8_SCHED;
;             PG8_STAGE_B(PG8_SB(1, 1), b21 + kstepB);
;             PG8_WAIT_V(6); PG8_BAR; PG8_MMA(1, 1, At, B1); PG8_BAR;
.LBB0_1123:
	v_add_u32_e32 v14, s56, v186
	ds_read_b128 v[2:5], v14
	ds_read_b128 v[6:9], v14 offset:1024
	ds_read_b128 v[10:13], v14 offset:2048
	ds_read_b128 v[14:17], v14 offset:3072
	s_and_b64 s[42:43], s[42:43], exec
	s_cselect_b32 s47, s29, s69
	s_cselect_b32 s46, s66, s39
	s_cselect_b32 s43, s67, s71
	s_cselect_b32 s42, s68, s70
	v_lshl_add_u64 v[18:19], v[174:175], 0, s[44:45]
	s_add_i32 m0, s49, 0xc000
	ds_read_b128 v[196:199], v189
	ds_read_b128 v[200:203], v189 offset:1024
	ds_read_b128 v[204:207], v189 offset:2048
	ds_read_b128 v[208:211], v189 offset:3072
	ds_read_b128 v[212:215], v189 offset:4096
	ds_read_b128 v[216:219], v189 offset:5120
	ds_read_b128 v[220:223], v189 offset:6144
	ds_read_b128 v[224:227], v189 offset:7168
	global_load_lds_dwordx4 v[18:19], off
	v_lshl_add_u64 v[18:19], v[176:177], 0, s[44:45]
	s_add_i32 m0, s49, 0xe000
	s_nop 0
	global_load_lds_dwordx4 v[18:19], off
	s_waitcnt lgkmcnt(8)
	s_barrier
	s_waitcnt lgkmcnt(0)
	s_nop 0
	s_waitcnt lgkmcnt(0)
	v_mfma_f32_16x16x128_f8f6f4 v[150:153], v[2:9], v[196:203], v[150:153]
	v_mfma_f32_16x16x128_f8f6f4 v[146:149], v[10:17], v[196:203], v[146:149]
	v_mfma_f32_16x16x128_f8f6f4 v[142:145], v[2:9], v[204:211], v[142:145]
	v_mfma_f32_16x16x128_f8f6f4 v[138:141], v[10:17], v[204:211], v[138:141]
	v_mfma_f32_16x16x128_f8f6f4 v[134:137], v[2:9], v[212:219], v[134:137]
	v_mfma_f32_16x16x128_f8f6f4 v[130:133], v[10:17], v[212:219], v[130:133]
	v_mfma_f32_16x16x128_f8f6f4 v[126:129], v[2:9], v[220:227], v[126:129]
	v_mfma_f32_16x16x128_f8f6f4 v[122:125], v[10:17], v[220:227], v[122:125]
	s_nop 0
	s_barrier
	s_add_i32 s44, s56, s48
	v_add_u32_e32 v167, s57, v186
	v_lshl_add_u64 v[178:179], s[46:47], 0, v[156:157]
	s_mov_b32 m0, s44
	ds_read_b128 v[18:21], v167
	ds_read_b128 v[22:25], v167 offset:1024
	ds_read_b128 v[228:231], v167 offset:2048
	ds_read_b128 v[232:235], v167 offset:3072
	global_load_lds_dwordx4 v[178:179], off
	v_lshl_add_u64 v[178:179], s[46:47], 0, v[154:155]
	s_add_i32 m0, s44, 0x2000
	s_nop 0
	global_load_lds_dwordx4 v[178:179], off
	s_barrier
	s_waitcnt lgkmcnt(0)
	s_nop 0
	s_waitcnt lgkmcnt(0)
	v_mfma_f32_16x16x128_f8f6f4 v[94:97], v[18:25], v[196:203], v[94:97]
	v_mfma_f32_16x16x128_f8f6f4 v[90:93], v[228:235], v[196:203], v[90:93]
	v_mfma_f32_16x16x128_f8f6f4 v[78:81], v[18:25], v[204:211], v[78:81]
	v_mfma_f32_16x16x128_f8f6f4 v[74:77], v[228:235], v[204:211], v[74:77]
	v_mfma_f32_16x16x128_f8f6f4 v[70:73], v[18:25], v[212:219], v[70:73]
	v_mfma_f32_16x16x128_f8f6f4 v[66:69], v[228:235], v[212:219], v[66:69]
	v_mfma_f32_16x16x128_f8f6f4 v[62:65], v[18:25], v[220:227], v[62:65]
	v_mfma_f32_16x16x128_f8f6f4 v[58:61], v[228:235], v[220:227], v[58:61]
	s_nop 0
	s_mov_b32 m0, s49
	s_barrier
	ds_read_b128 v[196:199], v189 offset:16384
	ds_read_b128 v[200:203], v189 offset:17408
	ds_read_b128 v[204:207], v189 offset:18432
	ds_read_b128 v[208:211], v189 offset:19456
	ds_read_b128 v[212:215], v189 offset:20480
	ds_read_b128 v[216:219], v189 offset:21504
	ds_read_b128 v[220:223], v189 offset:22528
	ds_read_b128 v[224:227], v189 offset:23552
	global_load_lds_dwordx4 v158, s[2:3]
	s_mov_b32 m0, s50
	v_mov_b32_e32 v171, v159
	global_load_lds_dwordx4 v170, s[2:3]
	s_barrier
	s_waitcnt lgkmcnt(0)
	v_lshl_add_u64 v[180:181], s[2:3], 0, v[158:159]
	v_lshl_add_u64 v[178:179], s[2:3], 0, v[170:171]
	s_nop 0
	s_waitcnt lgkmcnt(0)
	v_mfma_f32_16x16x128_f8f6f4 v[118:121], v[2:9], v[196:203], v[118:121]
	v_mfma_f32_16x16x128_f8f6f4 v[114:117], v[10:17], v[196:203], v[114:117]
	v_mfma_f32_16x16x128_f8f6f4 v[110:113], v[2:9], v[204:211], v[110:113]
	v_mfma_f32_16x16x128_f8f6f4 v[106:109], v[10:17], v[204:211], v[106:109]
	v_mfma_f32_16x16x128_f8f6f4 v[102:105], v[2:9], v[212:219], v[102:105]
	v_mfma_f32_16x16x128_f8f6f4 v[98:101], v[10:17], v[212:219], v[98:101]
	v_mfma_f32_16x16x128_f8f6f4 v[86:89], v[2:9], v[220:227], v[86:89]
	v_mfma_f32_16x16x128_f8f6f4 v[82:85], v[10:17], v[220:227], v[82:85]
	s_nop 0
	s_barrier
	s_add_i32 s44, s57, s48
	v_lshl_add_u64 v[2:3], s[42:43], 0, v[156:157]
	s_mov_b32 m0, s44
	s_nop 0
	global_load_lds_dwordx4 v[2:3], off
	v_lshl_add_u64 v[2:3], s[42:43], 0, v[154:155]
	s_add_i32 m0, s44, 0x2000
	s_nop 0
	global_load_lds_dwordx4 v[2:3], off
	s_waitcnt vmcnt(6)
	s_barrier
	s_nop 0
	v_mfma_f32_16x16x128_f8f6f4 v[54:57], v[18:25], v[196:203], v[54:57]
	v_mfma_f32_16x16x128_f8f6f4 v[50:53], v[228:235], v[196:203], v[50:53]
	v_mfma_f32_16x16x128_f8f6f4 v[46:49], v[18:25], v[204:211], v[46:49]
	v_mfma_f32_16x16x128_f8f6f4 v[42:45], v[228:235], v[204:211], v[42:45]
	v_mfma_f32_16x16x128_f8f6f4 v[38:41], v[18:25], v[212:219], v[38:41]
	v_mfma_f32_16x16x128_f8f6f4 v[34:37], v[228:235], v[212:219], v[34:37]
	v_mfma_f32_16x16x128_f8f6f4 v[30:33], v[18:25], v[220:227], v[30:33]
	v_mfma_f32_16x16x128_f8f6f4 v[26:29], v[228:235], v[220:227], v[26:29]
	s_nop 0
	s_add_i32 s73, 0, 0x18000
	v_add_u32_e32 v14, s73, v186
	s_barrier
; #define PG8_STAGE_B(bufoff, gbase) do { _Pragma("unroll") for (int _i = 0; _i < 2; ++_i) \
;         __builtin_amdgcn_global_load_lds((const unsigned*)((const char*)(gbase) + voffB[_i]), (LAS unsigned*)(lds + (bufoff) + ldsw + _i * 8192), 16, 0, 0); } while (0)
; #define PG8_STAGE_A(bufoff, AO, h, kb) do { _Pragma("unroll") for (int _i = 0; _i < 2; ++_i) \
;         __builtin_amdgcn_global_load_lds((const unsigned*)(S.A + (size_t)(AO)[h][_i] + (size_t)(kb)), (LAS unsigned*)(lds + (bufoff) + ldsw + _i * 8192), 16, 0, 0); } while (0)
; #define PG8_LDA(dst, b, h) do { _Pragma("unroll") for (int m = 0; m < 4; ++m) { dst[m].lo = *(const LAS i32x4*)(lds + PG8_SA(b, h) + aoff + m * 2048); dst[m].hi = *(const LAS i32x4*)(lds + PG8_SA(b, h) + aoff + m * 2048 + 1024); } } while (0)
; #define PG8_LDB(dst, b, h) do { _Pragma("unroll") for (int n = 0; n < 2; ++n) { dst[n].lo = *(const LAS i32x4*)(lds + PG8_SB(b, h) + boff + n * 2048); dst[n].hi = *(const LAS i32x4*)(lds + PG8_SB(b, h) + boff + n * 2048 + 1024); } } while (0)
; #define PG8_BAR __builtin_amdgcn_s_barrier()
; template <class P>
; __device__ __forceinline__ void gemm_phase(LAS unsigned char* lds, const P& S) {
;     ...
;             PG8_LDB(B0, 0, 0); PG8_SCHED; PG8_LDA(At, 0, 0); PG8_STAGE_A(PG8_SA(1, 1), ac, 1, k1);
;             PG8_WAIT_L(8); PG8_BAR; PG8_WAIT_L(0); PG8_MMA(0, 0, At, B0); PG8_BAR; PG8_SCHED;
;             PG8_LDB(B1, 0, 1); PG8_STAGE_B(PG8_SB(0, 0), b20);
;             PG8_BAR; PG8_WAIT_L(0); PG8_MMA(0, 1, At, B1); PG8_BAR;
;             PG8_LDA(At, 0, 1); PG8_STAGE_A(PG8_SA(0, 0), a2, 0, 0);
;             PG8_BAR; PG8_WAIT_L(0); PG8_MMA(1, 0, At, B0); PG8_BAR; PG8_SCHED;
;             PG8_STAGE_B(PG8_SB(0, 1), b21);
;             PG8_WAIT_V(6); PG8_BAR; PG8_MMA(1, 1, At, B1); PG8_BAR;
;             PG8_LDB(B0, 1, 0); PG8_SCHED; PG8_LDA(At, 1, 0); PG8_STAGE_A(PG8_SA(0, 1), a2, 1, 0);
;             PG8_WAIT_L(8); PG8_BAR; PG8_WAIT_L(0); PG8_MMA(0, 0, At, B0); PG8_BAR; PG8_SCHED;
;             PG8_LDB(B1, 1, 1); PG8_STAGE_B(PG8_SB(1, 0), b20 + kstepB);
;             PG8_BAR; PG8_WAIT_L(0); PG8_MMA(0, 1, At, B1); PG8_BAR;
;             PG8_LDA(At, 1, 1); PG8_STAGE_A(PG8_SA(1, 0), a2, 0, kstep);
;             PG8_BAR; PG8_WAIT_L(0); PG8_MMA(1, 0, At, B0); PG8_BAR; PG8_SCHED;
;             PG8_STAGE_B(PG8_SB(1, 1), b21 + kstepB);
;             PG8_WAIT_V(6); PG8_BAR; PG8_MMA(1, 1, At, B1); PG8_BAR;
	ds_read_b128 v[2:5], v14
	ds_read_b128 v[6:9], v14 offset:1024
	ds_read_b128 v[10:13], v14 offset:2048
	ds_read_b128 v[14:17], v14 offset:3072
	s_mov_b32 m0, s51
	ds_read_b128 v[18:21], v189 offset:32768
	ds_read_b128 v[22:25], v189 offset:33792
	ds_read_b128 v[196:199], v189 offset:34816
	ds_read_b128 v[200:203], v189 offset:35840
	ds_read_b128 v[204:207], v189 offset:36864
	ds_read_b128 v[208:211], v189 offset:37888
	ds_read_b128 v[212:215], v189 offset:38912
	ds_read_b128 v[216:219], v189 offset:39936
	global_load_lds_dwordx4 v192, s[2:3]
	s_mov_b32 m0, s52
	s_nop 0
	global_load_lds_dwordx4 v169, s[2:3]
	s_waitcnt lgkmcnt(8)
	s_barrier
	s_waitcnt lgkmcnt(0)
	s_nop 0
	s_waitcnt lgkmcnt(0)
	v_mfma_f32_16x16x128_f8f6f4 v[150:153], v[2:9], v[18:25], v[150:153]
	v_mfma_f32_16x16x128_f8f6f4 v[146:149], v[10:17], v[18:25], v[146:149]
	v_mfma_f32_16x16x128_f8f6f4 v[142:145], v[2:9], v[196:203], v[142:145]
	v_mfma_f32_16x16x128_f8f6f4 v[138:141], v[10:17], v[196:203], v[138:141]
	v_mfma_f32_16x16x128_f8f6f4 v[134:137], v[2:9], v[204:211], v[134:137]
	v_mfma_f32_16x16x128_f8f6f4 v[130:133], v[10:17], v[204:211], v[130:133]
	v_mfma_f32_16x16x128_f8f6f4 v[126:129], v[2:9], v[212:219], v[126:129]
	v_mfma_f32_16x16x128_f8f6f4 v[122:125], v[10:17], v[212:219], v[122:125]
	s_nop 0
	s_barrier
	s_add_i32 s74, 0, 0x1c000
	s_add_u32 s44, s46, 0x40000
	s_addc_u32 s45, s47, 0
	s_add_i32 s46, s73, s48
	v_add_u32_e32 v167, s74, v186
	v_lshl_add_u64 v[236:237], s[44:45], 0, v[156:157]
	s_mov_b32 m0, s46
	ds_read_b128 v[220:223], v167
	ds_read_b128 v[224:227], v167 offset:1024
	ds_read_b128 v[228:231], v167 offset:2048
	ds_read_b128 v[232:235], v167 offset:3072
	global_load_lds_dwordx4 v[236:237], off
	v_lshl_add_u64 v[236:237], s[44:45], 0, v[154:155]
	s_add_i32 m0, s46, 0x2000
	s_nop 0
	global_load_lds_dwordx4 v[236:237], off
	s_barrier
	s_waitcnt lgkmcnt(0)
	s_nop 0
	s_waitcnt lgkmcnt(0)
	v_mfma_f32_16x16x128_f8f6f4 v[94:97], v[220:227], v[18:25], v[94:97]
	v_mfma_f32_16x16x128_f8f6f4 v[90:93], v[228:235], v[18:25], v[90:93]
	v_mfma_f32_16x16x128_f8f6f4 v[78:81], v[220:227], v[196:203], v[78:81]
	v_mfma_f32_16x16x128_f8f6f4 v[74:77], v[228:235], v[196:203], v[74:77]
	v_mfma_f32_16x16x128_f8f6f4 v[70:73], v[220:227], v[204:211], v[70:73]
	v_mfma_f32_16x16x128_f8f6f4 v[66:69], v[228:235], v[204:211], v[66:69]
	v_mfma_f32_16x16x128_f8f6f4 v[62:65], v[220:227], v[212:219], v[62:65]
	v_mfma_f32_16x16x128_f8f6f4 v[58:61], v[228:235], v[212:219], v[58:61]
	s_nop 0
	s_mov_b32 m0, s53
	v_lshl_add_u64 v[180:181], v[180:181], 0, s[6:7]
	s_barrier
	ds_read_b128 v[18:21], v189 offset:49152
	ds_read_b128 v[22:25], v189 offset:50176
	ds_read_b128 v[196:199], v189 offset:51200
	ds_read_b128 v[200:203], v189 offset:52224
	ds_read_b128 v[204:207], v189 offset:53248
	ds_read_b128 v[208:211], v189 offset:54272
	ds_read_b128 v[212:215], v189 offset:55296
	ds_read_b128 v[216:219], v189 offset:56320
	global_load_lds_dwordx4 v[180:181], off
	v_lshl_add_u64 v[178:179], v[178:179], 0, s[6:7]
	s_mov_b32 m0, s54
	s_nop 0
	global_load_lds_dwordx4 v[178:179], off
	s_barrier
	s_waitcnt lgkmcnt(0)
	s_nop 0
	s_waitcnt lgkmcnt(0)
	v_mfma_f32_16x16x128_f8f6f4 v[118:121], v[2:9], v[18:25], v[118:121]
	v_mfma_f32_16x16x128_f8f6f4 v[114:117], v[10:17], v[18:25], v[114:117]
	v_mfma_f32_16x16x128_f8f6f4 v[110:113], v[2:9], v[196:203], v[110:113]
	v_mfma_f32_16x16x128_f8f6f4 v[106:109], v[10:17], v[196:203], v[106:109]
	v_mfma_f32_16x16x128_f8f6f4 v[102:105], v[2:9], v[204:211], v[102:105]
	v_mfma_f32_16x16x128_f8f6f4 v[98:101], v[10:17], v[204:211], v[98:101]
	v_mfma_f32_16x16x128_f8f6f4 v[86:89], v[2:9], v[212:219], v[86:89]
	v_mfma_f32_16x16x128_f8f6f4 v[82:85], v[10:17], v[212:219], v[82:85]
	s_nop 0
	s_barrier
	s_add_u32 s42, s42, 0x40000
	s_addc_u32 s43, s43, 0
	s_add_i32 s44, s74, s48
	v_lshl_add_u64 v[2:3], s[42:43], 0, v[156:157]
	s_mov_b32 m0, s44
	s_nop 0
	global_load_lds_dwordx4 v[2:3], off
	v_lshl_add_u64 v[2:3], s[42:43], 0, v[154:155]
	s_add_i32 m0, s44, 0x2000
	s_nop 0
	global_load_lds_dwordx4 v[2:3], off
	s_waitcnt vmcnt(6)
	s_barrier
	s_nop 0
	v_mfma_f32_16x16x128_f8f6f4 v[54:57], v[220:227], v[18:25], v[54:57]
	v_mfma_f32_16x16x128_f8f6f4 v[50:53], v[228:235], v[18:25], v[50:53]
	v_mfma_f32_16x16x128_f8f6f4 v[46:49], v[220:227], v[196:203], v[46:49]
	v_mfma_f32_16x16x128_f8f6f4 v[42:45], v[228:235], v[196:203], v[42:45]
	v_mfma_f32_16x16x128_f8f6f4 v[38:41], v[220:227], v[204:211], v[38:41]
	v_mfma_f32_16x16x128_f8f6f4 v[34:37], v[228:235], v[204:211], v[34:37]
	v_mfma_f32_16x16x128_f8f6f4 v[30:33], v[220:227], v[212:219], v[30:33]
	v_mfma_f32_16x16x128_f8f6f4 v[26:29], v[228:235], v[212:219], v[26:29]
	s_nop 0
	s_add_i32 s72, s72, 2
	s_add_u32 s39, s39, 0x80000
	s_addc_u32 s69, s69, 0
	s_add_u32 s70, s70, 0x80000
	s_addc_u32 s71, s71, 0
	s_cmp_gt_u32 s72, 13
	s_mov_b64 s[44:45], s[40:41]
	s_barrier
	s_cbranch_scc1 .LBB0_1119

; #define PG8_WAIT_V(n) asm volatile("s_waitcnt vmcnt(" #n ")" ::: "memory")
; #define PG8_BAR __builtin_amdgcn_s_barrier()
; template <class P>
; __device__ __forceinline__ void gemm_phase(LAS unsigned char* lds, const P& S) {
;     ...
;     PG8_WAIT_V(0);
;     if (wr == 0) PG8_BAR;
;     PG8_BAR;
.LBB0_1132:
	s_setprio 0
	v_readlane_b32 s68, v253, 11
	v_readlane_b32 s69, v253, 12
	s_barrier
	v_readlane_b32 s70, v253, 13
	v_readlane_b32 s71, v253, 14
